# attention: each step's vmcnt(0) for the next tile's LDS-DMA moved from in front of the exp block down to right before the step's barrier (wait at first consumer, 7.2)
# baseline (speedup 1.0000x reference)
.LBB0_237:
	v_and_b32_e32 v163, 63, v39
	v_lshlrev_b32_e32 v40, 4, v163
	v_lshlrev_b32_e32 v39, 3, v163
	v_and_b32_e32 v40, 0xc0, v40
	v_lshlrev_b32_e32 v41, 1, v163
	s_cmp_lg_u32 0, -1
	v_and_or_b32 v40, v39, 24, v40
	v_and_b32_e32 v41, 32, v41
	v_and_b32_e32 v39, 0x100, v39
	s_cselect_b32 s4, 0, 0
	v_or3_b32 v39, v40, v41, v39
	v_add_u32_e32 v166, s4, v39
	v_max_f32_e32 v39, v18, v19
	v_max3_f32 v39, v39, v20, v21
	v_max3_f32 v39, v39, v22, v23
	v_max3_f32 v39, v39, v24, v25
	v_max3_f32 v39, v39, v26, v27
	v_max3_f32 v39, v39, v28, v29
	v_max3_f32 v39, v39, v30, v31
	v_max3_f32 v39, v39, v32, v33
	v_max3_f32 v39, v39, v2, v3
	v_max3_f32 v39, v39, v4, v5
	v_max3_f32 v39, v39, v6, v7
	v_max3_f32 v39, v39, v8, v9
	v_max3_f32 v39, v39, v10, v11
	v_max3_f32 v39, v39, v12, v13
	v_max3_f32 v39, v39, v14, v15
	v_max3_f32 v39, v39, v16, v17
	v_mov_b32_e32 v40, v39
	s_nop 1
	v_permlane32_swap_b32_e32 v39, v40
	v_max_f32_e32 v39, v39, v40
	v_add_f32_e32 v40, 0x7149f2ca, v39
	s_add_i32 s83, s4, s86
	v_mul_f32_e32 v40, 0x3e000000, v40
	s_add_i32 s85, s83, 0x10000
	v_cmp_ge_f32_e32 vcc, s33, v40
	s_cmp_eq_u64 vcc, exec
	v_max_f32_e32 v39, 0xf149f2ca, v39
	v_sub_f32_e32 v40, 0xf149f2ca, v39
	s_cselect_b64 s[4:5], -1, 0
	v_mul_f32_e32 v40, 0x3e38aa3b, v40
	v_cndmask_b32_e64 v116, v39, v161, s[4:5]
	v_exp_f32_e32 v179, v40
	v_mul_f32_e32 v40, 0xbe38aa3b, v116
	v_pk_fma_f32 v[32:33], v[32:33], s[84:85], v[40:41] op_sel_hi:[1,0,0]
	v_pk_fma_f32 v[30:31], v[30:31], s[84:85], v[40:41] op_sel_hi:[1,0,0]
	v_pk_fma_f32 v[28:29], v[28:29], s[84:85], v[40:41] op_sel_hi:[1,0,0]
	v_pk_fma_f32 v[26:27], v[26:27], s[84:85], v[40:41] op_sel_hi:[1,0,0]
	v_pk_fma_f32 v[24:25], v[24:25], s[84:85], v[40:41] op_sel_hi:[1,0,0]
	v_pk_fma_f32 v[22:23], v[22:23], s[84:85], v[40:41] op_sel_hi:[1,0,0]
	v_pk_fma_f32 v[20:21], v[20:21], s[84:85], v[40:41] op_sel_hi:[1,0,0]
	v_pk_fma_f32 v[18:19], v[18:19], s[84:85], v[40:41] op_sel_hi:[1,0,0]
	v_exp_f32_e32 v58, v20
	v_exp_f32_e32 v56, v18
	v_exp_f32_e32 v57, v19
	v_exp_f32_e32 v59, v21
	v_exp_f32_e32 v60, v22
	v_exp_f32_e32 v61, v23
	v_exp_f32_e32 v62, v24
	v_exp_f32_e32 v63, v25
	v_exp_f32_e32 v26, v26
	v_exp_f32_e32 v27, v27
	v_exp_f32_e32 v28, v28
	v_exp_f32_e32 v29, v29
	v_exp_f32_e32 v30, v30
	v_exp_f32_e32 v31, v31
	v_exp_f32_e32 v32, v32
	v_exp_f32_e32 v33, v33
	v_pk_fma_f32 v[42:43], v[16:17], s[84:85], v[40:41] op_sel_hi:[1,0,0]
	v_pk_fma_f32 v[44:45], v[14:15], s[84:85], v[40:41] op_sel_hi:[1,0,0]
	v_pk_fma_f32 v[46:47], v[12:13], s[84:85], v[40:41] op_sel_hi:[1,0,0]
	v_pk_fma_f32 v[48:49], v[10:11], s[84:85], v[40:41] op_sel_hi:[1,0,0]
	v_pk_fma_f32 v[50:51], v[8:9], s[84:85], v[40:41] op_sel_hi:[1,0,0]
	v_pk_fma_f32 v[52:53], v[6:7], s[84:85], v[40:41] op_sel_hi:[1,0,0]
	v_pk_fma_f32 v[54:55], v[4:5], s[84:85], v[40:41] op_sel_hi:[1,0,0]
	v_pk_fma_f32 v[40:41], v[2:3], s[84:85], v[40:41] op_sel_hi:[1,0,0]
	s_waitcnt vmcnt(0)
	s_barrier
	s_add_u32 s6, s90, 0x80000
	s_addc_u32 s7, s91, 0
	s_mov_b32 m0, s85
	s_nop 0
	global_load_lds_dwordx4 v168, s[6:7] offset:0
	s_add_u32 s6, s92, 0x80000
	s_addc_u32 s7, s93, 0
	s_add_i32 s82, s83, 0x8000
	s_mov_b32 m0, s82
	s_nop 0
	global_load_lds_dwordx4 v169, s[6:7] offset:0
	s_add_i32 s83, s83, 0xa000
	s_mov_b32 m0, s83
	s_nop 0
	global_load_lds_dwordx4 v170, s[6:7] offset:0
	s_add_i32 s6, 0, 0x12000
	v_add_u32_e32 v10, s6, v35
	v_add_u32_e32 v175, v10, v37
	ds_read_b128 v[2:5], v175
	ds_read_b128 v[6:9], v175 offset:4096
	v_add_u32_e32 v176, v10, v38
	v_add_u32_e32 v177, v10, v36
	v_add_u32_e32 v178, v10, v34
	s_waitcnt lgkmcnt(1)
	v_mfma_f32_32x32x16_bf16 v[66:81], v[2:5], v[110:113], 0
	ds_read_b128 v[2:5], v176
	ds_read_b128 v[10:13], v176 offset:4096
	ds_read_b128 v[14:17], v177
	ds_read_b128 v[18:21], v177 offset:4096
	v_exp_f32_e32 v34, v40
	v_exp_f32_e32 v35, v41
	v_exp_f32_e32 v36, v54
	v_exp_f32_e32 v37, v55
	v_exp_f32_e32 v38, v52
	v_exp_f32_e32 v39, v53
	s_waitcnt lgkmcnt(4)
	v_mfma_f32_32x32x16_bf16 v[82:97], v[6:9], v[110:113], 0
	ds_read_b128 v[6:9], v178
	ds_read_b128 v[22:25], v178 offset:4096
	v_exp_f32_e32 v40, v50
	v_exp_f32_e32 v41, v51
	v_exp_f32_e32 v48, v48
	v_exp_f32_e32 v49, v49
	v_exp_f32_e32 v46, v46
	v_exp_f32_e32 v47, v47
	s_waitcnt lgkmcnt(5)
	v_mfma_f32_32x32x16_bf16 v[66:81], v[2:5], v[106:109], v[66:81]
	v_pk_add_f32 v[4:5], v[58:59], v[36:37]
	v_pk_add_f32 v[52:53], v[60:61], v[38:39]
	v_pk_add_f32 v[2:3], v[28:29], v[46:47]
	v_pk_add_f32 v[2:3], v[4:5], v[2:3]
	s_waitcnt lgkmcnt(4)
	v_mfma_f32_32x32x16_bf16 v[82:97], v[10:13], v[106:109], v[82:97]
	v_exp_f32_e32 v10, v44
	v_exp_f32_e32 v12, v42
	v_exp_f32_e32 v13, v43
	v_exp_f32_e32 v11, v45
	v_pk_add_f32 v[44:45], v[56:57], v[34:35]
	v_pk_add_f32 v[42:43], v[32:33], v[12:13]
	s_waitcnt lgkmcnt(3)
	v_mfma_f32_32x32x16_bf16 v[66:81], v[14:17], v[102:105], v[66:81]
	v_pk_add_f32 v[14:15], v[62:63], v[40:41]
	v_pk_add_f32 v[16:17], v[26:27], v[48:49]
	v_pk_add_f32 v[50:51], v[30:31], v[10:11]
	v_pk_add_f32 v[16:17], v[44:45], v[16:17]
	v_pk_add_f32 v[50:51], v[52:53], v[50:51]
	v_pk_add_f32 v[14:15], v[14:15], v[42:43]
	v_pk_add_f32 v[4:5], v[16:17], v[50:51]
	s_waitcnt lgkmcnt(2)
	v_mfma_f32_32x32x16_bf16 v[82:97], v[18:21], v[102:105], v[82:97]
	v_pk_add_f32 v[2:3], v[2:3], v[14:15]
	v_pk_add_f32 v[2:3], v[4:5], v[2:3]
	v_add_f32_e64 v114, v2, v3
	v_add_f32_e64 v115, v3, v2
	v_cvt_pk_bf16_f32 v2, v56, v57
	v_cvt_pk_bf16_f32 v3, v58, v59
	s_waitcnt lgkmcnt(1)
	v_mfma_f32_32x32x16_bf16 v[66:81], v[6:9], v[98:101], v[66:81]
	v_mov_b32_e32 v115, v114
	v_cvt_pk_bf16_f32 v4, v60, v61
	v_cvt_pk_bf16_f32 v5, v62, v63
	s_nop 1
	v_permlane32_swap_b32_e32 v114, v115
	v_permlane32_swap_b32_e32 v2, v4
	s_waitcnt lgkmcnt(0)
	v_mfma_f32_32x32x16_bf16 v[82:97], v[22:25], v[98:101], v[82:97]
	v_permlane32_swap_b32_e32 v3, v5
	v_cvt_pk_bf16_f32 v120, v26, v27
	v_cvt_pk_bf16_f32 v121, v28, v29
	v_cvt_pk_bf16_f32 v122, v30, v31
	v_cvt_pk_bf16_f32 v123, v32, v33
	v_cvt_pk_bf16_f32 v124, v34, v35
	v_cvt_pk_bf16_f32 v125, v36, v37
	v_cvt_pk_bf16_f32 v126, v38, v39
	v_cvt_pk_bf16_f32 v127, v40, v41
	v_cvt_pk_bf16_f32 v128, v48, v49
	v_cvt_pk_bf16_f32 v129, v46, v47
	v_cvt_pk_bf16_f32 v130, v10, v11
	v_cvt_pk_bf16_f32 v131, v12, v13
	s_nop 0
	v_permlane32_swap_b32_e32 v120, v122
	v_permlane32_swap_b32_e32 v121, v123
	v_permlane32_swap_b32_e32 v124, v126
	v_permlane32_swap_b32_e32 v125, v127
	v_permlane32_swap_b32_e32 v128, v130
	v_permlane32_swap_b32_e32 v129, v131
	ds_read_b64_tr_b16 v[6:7], v166 offset:0
	ds_read_b64_tr_b16 v[8:9], v166 offset:0x800
	ds_read_b64_tr_b16 v[10:11], v166 offset:0x1000
	ds_read_b64_tr_b16 v[12:13], v166 offset:0x1800
	ds_read_b64_tr_b16 v[14:15], v166 offset:0x2000
	ds_read_b64_tr_b16 v[16:17], v166 offset:0x2800
	ds_read_b64_tr_b16 v[34:35], v166 offset:0x3000
	ds_read_b64_tr_b16 v[36:37], v166 offset:0x3800
	ds_read_b64_tr_b16 v[38:39], v166 offset:0x200
	ds_read_b64_tr_b16 v[40:41], v166 offset:0xa00
	ds_read_b64_tr_b16 v[50:51], v166 offset:0x1200
	ds_read_b64_tr_b16 v[52:53], v166 offset:0x1a00
	ds_read_b64_tr_b16 v[54:55], v166 offset:0x2200
	ds_read_b64_tr_b16 v[56:57], v166 offset:0x2a00
	ds_read_b64_tr_b16 v[58:59], v166 offset:0x3200
	ds_read_b64_tr_b16 v[60:61], v166 offset:0x3a00
	s_waitcnt lgkmcnt(8)
	s_nop 0
	v_mfma_f32_32x32x16_bf16 v[18:33], v[2:5], v[6:9], 0
	v_mfma_f32_32x32x16_bf16 v[18:33], v[120:123], v[10:13], v[18:33]
	v_mfma_f32_32x32x16_bf16 v[18:33], v[124:127], v[14:17], v[18:33]
	v_mfma_f32_32x32x16_bf16 v[18:33], v[128:131], v[34:37], v[18:33]
	ds_read_b64_tr_b16 v[6:7], v166 offset:0x400
	ds_read_b64_tr_b16 v[8:9], v166 offset:0xc00
	ds_read_b64_tr_b16 v[10:11], v166 offset:0x1400
	ds_read_b64_tr_b16 v[12:13], v166 offset:0x1c00
	ds_read_b64_tr_b16 v[14:15], v166 offset:0x2400
	ds_read_b64_tr_b16 v[16:17], v166 offset:0x2c00
	ds_read_b64_tr_b16 v[132:133], v166 offset:0x3400
	ds_read_b64_tr_b16 v[134:135], v166 offset:0x3c00
	s_waitcnt lgkmcnt(8)
	v_mfma_f32_32x32x16_bf16 v[34:49], v[2:5], v[38:41], 0
	v_mfma_f32_32x32x16_bf16 v[34:49], v[120:123], v[50:53], v[34:49]
	v_mfma_f32_32x32x16_bf16 v[34:49], v[124:127], v[54:57], v[34:49]
	v_mfma_f32_32x32x16_bf16 v[34:49], v[128:131], v[58:61], v[34:49]
	ds_read_b64_tr_b16 v[140:141], v166 offset:0x600
	ds_read_b64_tr_b16 v[142:143], v166 offset:0xe00
	ds_read_b64_tr_b16 v[144:145], v166 offset:0x1600
	ds_read_b64_tr_b16 v[146:147], v166 offset:0x1e00
	ds_read_b64_tr_b16 v[148:149], v166 offset:0x2600
	ds_read_b64_tr_b16 v[150:151], v166 offset:0x2e00
	ds_read_b64_tr_b16 v[152:153], v166 offset:0x3600
	ds_read_b64_tr_b16 v[154:155], v166 offset:0x3e00
	s_waitcnt lgkmcnt(8)
	v_mfma_f32_32x32x16_bf16 v[50:65], v[2:5], v[6:9], 0
	v_mfma_f32_32x32x16_bf16 v[50:65], v[120:123], v[10:13], v[50:65]
	v_mfma_f32_32x32x16_bf16 v[50:65], v[124:127], v[14:17], v[50:65]
	v_mfma_f32_32x32x16_bf16 v[50:65], v[128:131], v[132:135], v[50:65]
	s_waitcnt lgkmcnt(0)
	v_mfma_f32_32x32x16_bf16 v[2:17], v[2:5], v[140:143], 0
	s_cmpk_gt_i32 s77, 0x7e
	v_mfma_f32_32x32x16_bf16 v[2:17], v[120:123], v[144:147], v[2:17]
	v_mfma_f32_32x32x16_bf16 v[2:17], v[124:127], v[148:151], v[2:17]
	v_mfma_f32_32x32x16_bf16 v[2:17], v[128:131], v[152:155], v[2:17]
	s_cbranch_scc1 .LBB0_239
	s_movk_i32 s60, 0x5a
	s_movk_i32 s62, 0x5b
	v_cmp_gt_i32_e64 s[60:61], s60, v167
	v_cmp_gt_i32_e64 s[62:63], s62, v167
	s_and_b64 s[60:61], s[62:63], s[60:61]
	s_movk_i32 s28, 0x58
	v_cndmask_b32_e64 v81, v81, v160, s[62:63]
	s_movk_i32 s62, 0x59
	v_cmp_gt_i32_e64 s[62:63], s62, v167
	s_movk_i32 s26, 0x53
	v_cmp_gt_i32_e64 s[58:59], s28, v167
	v_cndmask_b32_e64 v80, v80, v160, s[60:61]
	s_and_b64 s[60:61], s[60:61], s[62:63]
	s_movk_i32 s24, 0x52
	v_cmp_gt_i32_e64 s[56:57], s26, v167
	s_and_b64 s[58:59], s[60:61], s[58:59]
	s_movk_i32 s22, 0x51
	v_cmp_gt_i32_e64 s[54:55], s24, v167
	s_and_b64 s[56:57], s[58:59], s[56:57]
	s_movk_i32 s20, 0x50
	v_cmp_gt_i32_e64 s[52:53], s22, v167
	s_and_b64 s[54:55], s[56:57], s[54:55]
	s_movk_i32 s18, 0x4b
	v_cmp_gt_i32_e64 s[50:51], s20, v167
	s_and_b64 s[52:53], s[54:55], s[52:53]
	s_movk_i32 s16, 0x4a
	v_cmp_gt_i32_e64 s[48:49], s18, v167
	s_and_b64 s[50:51], s[52:53], s[50:51]
	s_movk_i32 s14, 0x49
	v_cmp_gt_i32_e64 s[44:45], s16, v167
	s_and_b64 s[48:49], s[50:51], s[48:49]
	s_movk_i32 s12, 0x48
	v_cmp_gt_i32_e64 s[42:43], s14, v167
	s_and_b64 s[44:45], s[48:49], s[44:45]
	s_movk_i32 s10, 0x43
	v_cmp_gt_i32_e64 s[40:41], s12, v167
	s_and_b64 s[42:43], s[44:45], s[42:43]
	s_movk_i32 s6, 0x60
	s_movk_i32 s8, 0x42
	v_cmp_gt_i32_e64 s[38:39], s10, v167
	s_and_b64 s[40:41], s[42:43], s[40:41]
	v_cmp_gt_i32_e32 vcc, s6, v167
	s_movk_i32 s6, 0x41
	v_cmp_gt_i32_e64 s[36:37], s8, v167
	s_and_b64 s[38:39], s[40:41], s[38:39]
	v_cmp_gt_i32_e64 s[34:35], s6, v167
	s_and_b64 s[36:37], s[38:39], s[36:37]
	v_cmp_gt_i32_e64 s[30:31], 64, v167
	s_and_b64 s[34:35], s[36:37], s[34:35]
	s_and_b64 s[30:31], s[34:35], s[30:31]
	v_cndmask_b32_e64 v79, v79, v160, s[60:61]
	s_movk_i32 s60, 0x7a
	v_cndmask_b32_e64 v66, v66, v160, s[30:31]
	s_movk_i32 s30, 0x7b
	s_movk_i32 s62, 0x79
	v_cmp_gt_i32_e64 s[60:61], s60, v167
	v_cmp_gt_i32_e64 s[30:31], s30, v167
	s_movk_i32 s28, 0x78
	v_cmp_gt_i32_e64 s[62:63], s62, v167
	v_cndmask_b32_e64 v97, v97, v160, s[30:31]
	s_and_b64 s[30:31], s[30:31], s[60:61]
	s_movk_i32 s26, 0x73
	v_cmp_gt_i32_e64 s[28:29], s28, v167
	v_cndmask_b32_e64 v96, v96, v160, s[30:31]
	s_and_b64 s[30:31], s[30:31], s[62:63]
	s_movk_i32 s24, 0x72
	v_cmp_gt_i32_e64 s[26:27], s26, v167
	s_and_b64 s[28:29], s[30:31], s[28:29]
	s_movk_i32 s22, 0x71
	v_cmp_gt_i32_e64 s[24:25], s24, v167
	s_and_b64 s[26:27], s[28:29], s[26:27]
	v_cmp_gt_i32_e64 s[22:23], s22, v167
	s_and_b64 s[24:25], s[26:27], s[24:25]
	s_movk_i32 s18, 0x6b
	v_cmp_gt_i32_e64 s[20:21], s69, v167
	s_and_b64 s[22:23], s[24:25], s[22:23]
	s_movk_i32 s16, 0x6a
	v_cmp_gt_i32_e64 s[18:19], s18, v167
	s_and_b64 s[20:21], s[22:23], s[20:21]
	s_movk_i32 s14, 0x69
	v_cmp_gt_i32_e64 s[16:17], s16, v167
	s_and_b64 s[18:19], s[20:21], s[18:19]
	s_movk_i32 s12, 0x68
	v_cmp_gt_i32_e64 s[14:15], s14, v167
	s_and_b64 s[16:17], s[18:19], s[16:17]
	s_movk_i32 s10, 0x63
	v_cmp_gt_i32_e64 s[12:13], s12, v167
	s_and_b64 s[14:15], s[16:17], s[14:15]
	s_movk_i32 s8, 0x62
	v_cmp_gt_i32_e64 s[10:11], s10, v167
	s_and_b64 s[12:13], s[14:15], s[12:13]
	s_movk_i32 s6, 0x61
	v_cmp_gt_i32_e64 s[8:9], s8, v167
	s_and_b64 s[10:11], s[12:13], s[10:11]
	v_cmp_gt_i32_e64 s[6:7], s6, v167
	s_and_b64 s[8:9], s[10:11], s[8:9]
	s_and_b64 s[6:7], s[8:9], s[6:7]
	s_and_b64 vcc, s[6:7], vcc
	v_cndmask_b32_e64 v78, v78, v160, s[58:59]
	v_cndmask_b32_e64 v77, v77, v160, s[56:57]
	v_cndmask_b32_e64 v76, v76, v160, s[54:55]
	v_cndmask_b32_e64 v75, v75, v160, s[52:53]
	v_cndmask_b32_e64 v74, v74, v160, s[50:51]
	v_cndmask_b32_e64 v73, v73, v160, s[48:49]
	v_cndmask_b32_e64 v72, v72, v160, s[44:45]
	v_cndmask_b32_e64 v71, v71, v160, s[42:43]
	v_cndmask_b32_e64 v70, v70, v160, s[40:41]
	v_cndmask_b32_e64 v69, v69, v160, s[38:39]
	v_cndmask_b32_e64 v68, v68, v160, s[36:37]
	v_cndmask_b32_e64 v67, v67, v160, s[34:35]
	v_cndmask_b32_e64 v95, v95, v160, s[30:31]
	v_cndmask_b32_e64 v94, v94, v160, s[28:29]
	v_cndmask_b32_e64 v93, v93, v160, s[26:27]
	v_cndmask_b32_e64 v92, v92, v160, s[24:25]
	v_cndmask_b32_e64 v91, v91, v160, s[22:23]
	v_cndmask_b32_e64 v90, v90, v160, s[20:21]
	v_cndmask_b32_e64 v89, v89, v160, s[18:19]
	v_cndmask_b32_e64 v88, v88, v160, s[16:17]
	v_cndmask_b32_e64 v87, v87, v160, s[14:15]
	v_cndmask_b32_e64 v86, v86, v160, s[12:13]
	v_cndmask_b32_e64 v85, v85, v160, s[10:11]
	v_cndmask_b32_e64 v84, v84, v160, s[8:9]
	v_cndmask_b32_e64 v83, v83, v160, s[6:7]
	v_cndmask_b32_e32 v82, v82, v160, vcc

.LBB0_243:
	v_cndmask_b32_e64 v120, v117, v116, s[6:7]
	v_mul_f32_e32 v116, 0xbe38aa3b, v120
	v_pk_fma_f32 v[80:81], v[80:81], s[84:85], v[116:117] op_sel_hi:[1,0,0]
	v_pk_fma_f32 v[78:79], v[78:79], s[84:85], v[116:117] op_sel_hi:[1,0,0]
	v_pk_fma_f32 v[76:77], v[76:77], s[84:85], v[116:117] op_sel_hi:[1,0,0]
	v_pk_fma_f32 v[74:75], v[74:75], s[84:85], v[116:117] op_sel_hi:[1,0,0]
	v_pk_fma_f32 v[72:73], v[72:73], s[84:85], v[116:117] op_sel_hi:[1,0,0]
	v_pk_fma_f32 v[70:71], v[70:71], s[84:85], v[116:117] op_sel_hi:[1,0,0]
	v_pk_fma_f32 v[68:69], v[68:69], s[84:85], v[116:117] op_sel_hi:[1,0,0]
	v_pk_fma_f32 v[66:67], v[66:67], s[84:85], v[116:117] op_sel_hi:[1,0,0]
	v_pk_fma_f32 v[148:149], v[96:97], s[84:85], v[116:117] op_sel_hi:[1,0,0]
	v_pk_fma_f32 v[150:151], v[94:95], s[84:85], v[116:117] op_sel_hi:[1,0,0]
	v_pk_fma_f32 v[152:153], v[92:93], s[84:85], v[116:117] op_sel_hi:[1,0,0]
	v_pk_fma_f32 v[154:155], v[90:91], s[84:85], v[116:117] op_sel_hi:[1,0,0]
	v_pk_fma_f32 v[180:181], v[88:89], s[84:85], v[116:117] op_sel_hi:[1,0,0]
	v_pk_fma_f32 v[184:185], v[86:87], s[84:85], v[116:117] op_sel_hi:[1,0,0]
	v_pk_fma_f32 v[186:187], v[84:85], s[84:85], v[116:117] op_sel_hi:[1,0,0]
	v_pk_fma_f32 v[116:117], v[82:83], s[84:85], v[116:117] op_sel_hi:[1,0,0]
	v_exp_f32_e32 v196, v66
	v_exp_f32_e32 v197, v67
	v_exp_f32_e32 v198, v68
	v_exp_f32_e32 v199, v69
	v_exp_f32_e32 v200, v70
	v_exp_f32_e32 v201, v71
	v_exp_f32_e32 v202, v72
	v_exp_f32_e32 v203, v73
	v_exp_f32_e32 v204, v74
	v_exp_f32_e32 v205, v75
	v_exp_f32_e32 v206, v76
	v_exp_f32_e32 v207, v77
	v_exp_f32_e32 v208, v78
	v_exp_f32_e32 v209, v79
	v_exp_f32_e32 v210, v80
	v_exp_f32_e32 v211, v81
	s_waitcnt vmcnt(0)
	s_barrier
	s_add_u32 s6, s90, 0xc0000
	s_addc_u32 s7, s91, 0
	s_mov_b32 m0, s81
	s_nop 0
	global_load_lds_dwordx4 v168, s[6:7] offset:0
	s_add_u32 s6, s92, 0xc0000
	s_addc_u32 s7, s93, 0
	s_cmp_lg_u32 0, -1
	s_cselect_b32 s1, 0, 0
	s_add_i32 s79, s1, s86
	s_add_i32 s78, s79, 0xc000
	s_mov_b32 m0, s78
	s_nop 0
	global_load_lds_dwordx4 v169, s[6:7] offset:0
	s_add_i32 s79, s79, 0xe000
	s_mov_b32 m0, s79
	s_nop 0
	global_load_lds_dwordx4 v170, s[6:7] offset:0
	ds_read_b128 v[66:69], v171
	ds_read_b128 v[70:73], v171 offset:4096
	ds_read_b128 v[122:125], v172
	ds_read_b128 v[126:129], v172 offset:4096
	ds_read_b128 v[130:133], v173
	ds_read_b128 v[134:137], v173 offset:4096
	ds_read_b128 v[140:143], v174
	ds_read_b128 v[144:147], v174 offset:4096
	s_waitcnt lgkmcnt(7)
	v_mfma_f32_32x32x16_bf16 v[82:97], v[66:69], v[110:113], 0
	v_exp_f32_e32 v212, v116
	v_exp_f32_e32 v213, v117
	v_exp_f32_e32 v186, v186
	v_exp_f32_e32 v187, v187
	v_exp_f32_e32 v184, v184
	v_exp_f32_e32 v185, v185
	v_exp_f32_e32 v180, v180
	s_waitcnt lgkmcnt(6)
	v_mfma_f32_32x32x16_bf16 v[66:81], v[70:73], v[110:113], 0
	v_exp_f32_e32 v181, v181
	v_exp_f32_e32 v154, v154
	v_exp_f32_e32 v155, v155
	v_exp_f32_e32 v152, v152
	v_exp_f32_e32 v153, v153
	v_exp_f32_e32 v150, v150
	v_exp_f32_e32 v151, v151
	s_waitcnt lgkmcnt(5)
	v_mfma_f32_32x32x16_bf16 v[82:97], v[122:125], v[106:109], v[82:97]
	v_exp_f32_e32 v148, v148
	v_exp_f32_e32 v149, v149
	v_pk_add_f32 v[116:117], v[206:207], v[152:153]
	v_pk_add_f32 v[122:123], v[198:199], v[186:187]
	v_pk_add_f32 v[214:215], v[196:197], v[212:213]
	v_pk_add_f32 v[124:125], v[210:211], v[148:149]
	v_pk_add_f32 v[216:217], v[208:209], v[150:151]
	s_waitcnt lgkmcnt(4)
	v_mfma_f32_32x32x16_bf16 v[66:81], v[126:129], v[106:109], v[66:81]
	v_pk_add_f32 v[126:127], v[202:203], v[180:181]
	v_pk_add_f32 v[128:129], v[204:205], v[154:155]
	v_pk_add_f32 v[218:219], v[200:201], v[184:185]
	v_pk_add_f32 v[128:129], v[214:215], v[128:129]
	v_pk_add_f32 v[216:217], v[218:219], v[216:217]
	v_pk_add_f32 v[124:125], v[126:127], v[124:125]
	v_pk_add_f32 v[116:117], v[122:123], v[116:117]
	s_waitcnt lgkmcnt(3)
	v_mfma_f32_32x32x16_bf16 v[82:97], v[130:133], v[102:105], v[82:97]
	v_pk_add_f32 v[116:117], v[116:117], v[124:125]
	v_pk_add_f32 v[122:123], v[128:129], v[216:217]
	v_pk_add_f32 v[116:117], v[122:123], v[116:117]
	v_cvt_pk_bf16_f32 v122, v196, v197
	v_cvt_pk_bf16_f32 v123, v198, v199
	v_cvt_pk_bf16_f32 v124, v200, v201
	s_waitcnt lgkmcnt(2)
	v_mfma_f32_32x32x16_bf16 v[66:81], v[134:137], v[102:105], v[66:81]
	v_pk_add_f32 v[116:117], v[116:117], v[116:117] op_sel:[0,1] op_sel_hi:[1,0]
	v_cvt_pk_bf16_f32 v125, v202, v203
	v_cvt_pk_bf16_f32 v126, v204, v205
	v_cvt_pk_bf16_f32 v127, v206, v207
	v_cvt_pk_bf16_f32 v128, v208, v209
	v_cvt_pk_bf16_f32 v129, v210, v211
	s_nop 0
	v_mov_b32_e32 v117, v116
	s_waitcnt lgkmcnt(1)
	v_mfma_f32_32x32x16_bf16 v[82:97], v[140:143], v[98:101], v[82:97]
	v_permlane32_swap_b32_e32 v116, v117
	v_cvt_pk_bf16_f32 v130, v212, v213
	v_cvt_pk_bf16_f32 v131, v186, v187
	v_cvt_pk_bf16_f32 v132, v184, v185
	v_cvt_pk_bf16_f32 v133, v180, v181
	v_cvt_pk_bf16_f32 v134, v154, v155
	s_waitcnt lgkmcnt(0)
	v_mfma_f32_32x32x16_bf16 v[66:81], v[144:147], v[98:101], v[66:81]
	v_cvt_pk_bf16_f32 v135, v152, v153
	v_cvt_pk_bf16_f32 v136, v150, v151
	v_cvt_pk_bf16_f32 v137, v148, v149
	v_permlane32_swap_b32_e32 v122, v124
	v_permlane32_swap_b32_e32 v123, v125
	v_permlane32_swap_b32_e32 v126, v128
	v_permlane32_swap_b32_e32 v127, v129
	v_permlane32_swap_b32_e32 v130, v132
	v_permlane32_swap_b32_e32 v131, v133
	v_permlane32_swap_b32_e32 v134, v136
	v_permlane32_swap_b32_e32 v135, v137
	ds_read_b64_tr_b16 v[140:141], v166 offset:0x4000
	ds_read_b64_tr_b16 v[142:143], v166 offset:0x4800
	ds_read_b64_tr_b16 v[144:145], v166 offset:0x5000
	ds_read_b64_tr_b16 v[146:147], v166 offset:0x5800
	ds_read_b64_tr_b16 v[148:149], v166 offset:0x6000
	ds_read_b64_tr_b16 v[150:151], v166 offset:0x6800
	ds_read_b64_tr_b16 v[152:153], v166 offset:0x7000
	ds_read_b64_tr_b16 v[154:155], v166 offset:0x7800
	ds_read_b64_tr_b16 v[184:185], v166 offset:0x4200
	ds_read_b64_tr_b16 v[186:187], v166 offset:0x4a00
	ds_read_b64_tr_b16 v[196:197], v166 offset:0x5200
	ds_read_b64_tr_b16 v[198:199], v166 offset:0x5a00
	ds_read_b64_tr_b16 v[200:201], v166 offset:0x6200
	ds_read_b64_tr_b16 v[202:203], v166 offset:0x6a00
	ds_read_b64_tr_b16 v[204:205], v166 offset:0x7200
	ds_read_b64_tr_b16 v[206:207], v166 offset:0x7a00
	s_waitcnt lgkmcnt(8)
	s_nop 0
	v_mfma_f32_32x32x16_bf16 v[18:33], v[122:125], v[140:143], v[18:33]
	v_mfma_f32_32x32x16_bf16 v[18:33], v[126:129], v[144:147], v[18:33]
	v_mfma_f32_32x32x16_bf16 v[18:33], v[130:133], v[148:151], v[18:33]
	v_mfma_f32_32x32x16_bf16 v[18:33], v[134:137], v[152:155], v[18:33]
	ds_read_b64_tr_b16 v[140:141], v166 offset:0x4400
	ds_read_b64_tr_b16 v[142:143], v166 offset:0x4c00
	ds_read_b64_tr_b16 v[144:145], v166 offset:0x5400
	ds_read_b64_tr_b16 v[146:147], v166 offset:0x5c00
	ds_read_b64_tr_b16 v[148:149], v166 offset:0x6400
	ds_read_b64_tr_b16 v[150:151], v166 offset:0x6c00
	ds_read_b64_tr_b16 v[152:153], v166 offset:0x7400
	ds_read_b64_tr_b16 v[154:155], v166 offset:0x7c00
	s_waitcnt lgkmcnt(8)
	v_mfma_f32_32x32x16_bf16 v[34:49], v[122:125], v[184:187], v[34:49]
	v_mfma_f32_32x32x16_bf16 v[34:49], v[126:129], v[196:199], v[34:49]
	v_mfma_f32_32x32x16_bf16 v[34:49], v[130:133], v[200:203], v[34:49]
	v_mfma_f32_32x32x16_bf16 v[34:49], v[134:137], v[204:207], v[34:49]
	ds_read_b64_tr_b16 v[184:185], v166 offset:0x4600
	ds_read_b64_tr_b16 v[186:187], v166 offset:0x4e00
	ds_read_b64_tr_b16 v[196:197], v166 offset:0x5600
	ds_read_b64_tr_b16 v[198:199], v166 offset:0x5e00
	ds_read_b64_tr_b16 v[200:201], v166 offset:0x6600
	ds_read_b64_tr_b16 v[202:203], v166 offset:0x6e00
	ds_read_b64_tr_b16 v[204:205], v166 offset:0x7600
	ds_read_b64_tr_b16 v[206:207], v166 offset:0x7e00
	s_waitcnt lgkmcnt(8)
	v_mfma_f32_32x32x16_bf16 v[50:65], v[122:125], v[140:143], v[50:65]
	v_mfma_f32_32x32x16_bf16 v[50:65], v[126:129], v[144:147], v[50:65]
	v_mfma_f32_32x32x16_bf16 v[50:65], v[130:133], v[148:151], v[50:65]
	v_mfma_f32_32x32x16_bf16 v[50:65], v[134:137], v[152:155], v[50:65]
	s_waitcnt lgkmcnt(0)
	v_mfma_f32_32x32x16_bf16 v[2:17], v[122:125], v[184:187], v[2:17]
	s_cmpk_gt_i32 s77, 0xbe
	v_mfma_f32_32x32x16_bf16 v[2:17], v[126:129], v[196:199], v[2:17]
	v_mfma_f32_32x32x16_bf16 v[2:17], v[130:133], v[200:203], v[2:17]
	v_mfma_f32_32x32x16_bf16 v[2:17], v[134:137], v[204:207], v[2:17]
	s_cbranch_scc1 .LBB0_245
	s_movk_i32 s1, 0x80
	v_cmp_gt_i32_e64 s[30:31], s1, v167
	s_movk_i32 s1, 0xa0
	v_cmp_gt_i32_e32 vcc, s1, v167
	s_movk_i32 s1, 0x81
	v_cmp_gt_i32_e64 s[34:35], s1, v167
	s_movk_i32 s1, 0xa1
	v_cmp_gt_i32_e64 s[6:7], s1, v167
	s_movk_i32 s1, 0x82
	v_cmp_gt_i32_e64 s[36:37], s1, v167
	s_movk_i32 s1, 0xa2
	v_cmp_gt_i32_e64 s[8:9], s1, v167
	s_movk_i32 s1, 0x83
	v_cmp_gt_i32_e64 s[38:39], s1, v167
	s_movk_i32 s1, 0xa3
	v_cmp_gt_i32_e64 s[10:11], s1, v167
	s_movk_i32 s1, 0x88
	v_cmp_gt_i32_e64 s[40:41], s1, v167
	s_movk_i32 s1, 0xa8
	v_cmp_gt_i32_e64 s[12:13], s1, v167
	s_movk_i32 s1, 0x89
	v_cmp_gt_i32_e64 s[42:43], s1, v167
	s_movk_i32 s1, 0xa9
	v_cmp_gt_i32_e64 s[14:15], s1, v167
	s_movk_i32 s1, 0x8a
	v_cmp_gt_i32_e64 s[44:45], s1, v167
	s_movk_i32 s1, 0xaa
	v_cmp_gt_i32_e64 s[16:17], s1, v167
	s_movk_i32 s1, 0x8b
	v_cmp_gt_i32_e64 s[48:49], s1, v167
	s_movk_i32 s1, 0xab
	v_cmp_gt_i32_e64 s[18:19], s1, v167
	s_movk_i32 s1, 0x90
	v_cmp_gt_i32_e64 s[50:51], s1, v167
	s_movk_i32 s1, 0xb0
	v_cmp_gt_i32_e64 s[20:21], s1, v167
	s_movk_i32 s1, 0x91
	v_cmp_gt_i32_e64 s[52:53], s1, v167
	s_movk_i32 s1, 0xb1
	v_cmp_gt_i32_e64 s[22:23], s1, v167
	s_movk_i32 s1, 0x92
	v_cmp_gt_i32_e64 s[54:55], s1, v167
	s_movk_i32 s1, 0xb2
	v_cmp_gt_i32_e64 s[24:25], s1, v167
	s_movk_i32 s1, 0x93
	v_cmp_gt_i32_e64 s[56:57], s1, v167
	s_movk_i32 s1, 0xb3
	v_cmp_gt_i32_e64 s[26:27], s1, v167
	s_movk_i32 s1, 0x98
	v_cmp_gt_i32_e64 s[58:59], s1, v167
	s_movk_i32 s1, 0xb8
	v_cmp_gt_i32_e64 s[28:29], s1, v167
	s_movk_i32 s1, 0x9a
	v_cmp_gt_i32_e64 s[60:61], s1, v167
	s_movk_i32 s1, 0x9b
	v_cmp_gt_i32_e64 s[62:63], s1, v167
	s_movk_i32 s1, 0x99
	s_and_b64 s[60:61], s[62:63], s[60:61]
	v_cndmask_b32_e64 v97, v97, v160, s[62:63]
	v_cmp_gt_i32_e64 s[62:63], s1, v167
	v_cndmask_b32_e64 v96, v96, v160, s[60:61]
	s_and_b64 s[60:61], s[60:61], s[62:63]
	s_and_b64 s[58:59], s[60:61], s[58:59]
	s_and_b64 s[56:57], s[58:59], s[56:57]
	s_and_b64 s[54:55], s[56:57], s[54:55]
	s_and_b64 s[52:53], s[54:55], s[52:53]
	s_and_b64 s[50:51], s[52:53], s[50:51]
	s_and_b64 s[48:49], s[50:51], s[48:49]
	s_and_b64 s[44:45], s[48:49], s[44:45]
	s_and_b64 s[42:43], s[44:45], s[42:43]
	s_and_b64 s[40:41], s[42:43], s[40:41]
	s_and_b64 s[38:39], s[40:41], s[38:39]
	s_movk_i32 s1, 0xb9
	s_and_b64 s[36:37], s[38:39], s[36:37]
	v_cmp_gt_i32_e64 s[62:63], s1, v167
	s_movk_i32 s1, 0xba
	s_and_b64 s[34:35], s[36:37], s[34:35]
	v_cndmask_b32_e64 v95, v95, v160, s[60:61]
	v_cmp_gt_i32_e64 s[60:61], s1, v167
	s_and_b64 s[30:31], s[34:35], s[30:31]
	s_movk_i32 s1, 0xbb
	v_cndmask_b32_e64 v82, v82, v160, s[30:31]
	v_cmp_gt_i32_e64 s[30:31], s1, v167
	v_cndmask_b32_e64 v94, v94, v160, s[58:59]
	v_cndmask_b32_e64 v93, v93, v160, s[56:57]
	v_cndmask_b32_e64 v81, v81, v160, s[30:31]
	s_and_b64 s[30:31], s[30:31], s[60:61]
	v_cndmask_b32_e64 v80, v80, v160, s[30:31]
	s_and_b64 s[30:31], s[30:31], s[62:63]
	s_and_b64 s[28:29], s[30:31], s[28:29]
	s_and_b64 s[26:27], s[28:29], s[26:27]
	s_and_b64 s[24:25], s[26:27], s[24:25]
	s_and_b64 s[22:23], s[24:25], s[22:23]
	s_and_b64 s[20:21], s[22:23], s[20:21]
	s_and_b64 s[18:19], s[20:21], s[18:19]
	s_and_b64 s[16:17], s[18:19], s[16:17]
	s_and_b64 s[14:15], s[16:17], s[14:15]
	s_and_b64 s[12:13], s[14:15], s[12:13]
	s_and_b64 s[10:11], s[12:13], s[10:11]
	s_and_b64 s[8:9], s[10:11], s[8:9]
	s_and_b64 s[6:7], s[8:9], s[6:7]
	s_and_b64 vcc, s[6:7], vcc
	v_cndmask_b32_e64 v92, v92, v160, s[54:55]
	v_cndmask_b32_e64 v91, v91, v160, s[52:53]
	v_cndmask_b32_e64 v90, v90, v160, s[50:51]
	v_cndmask_b32_e64 v89, v89, v160, s[48:49]
	v_cndmask_b32_e64 v88, v88, v160, s[44:45]
	v_cndmask_b32_e64 v87, v87, v160, s[42:43]
	v_cndmask_b32_e64 v86, v86, v160, s[40:41]
	v_cndmask_b32_e64 v85, v85, v160, s[38:39]
	v_cndmask_b32_e64 v84, v84, v160, s[36:37]
	v_cndmask_b32_e64 v83, v83, v160, s[34:35]
	v_cndmask_b32_e64 v79, v79, v160, s[30:31]
	v_cndmask_b32_e64 v78, v78, v160, s[28:29]
	v_cndmask_b32_e64 v77, v77, v160, s[26:27]
	v_cndmask_b32_e64 v76, v76, v160, s[24:25]
	v_cndmask_b32_e64 v75, v75, v160, s[22:23]
	v_cndmask_b32_e64 v74, v74, v160, s[20:21]
	v_cndmask_b32_e64 v73, v73, v160, s[18:19]
	v_cndmask_b32_e64 v72, v72, v160, s[16:17]
	v_cndmask_b32_e64 v71, v71, v160, s[14:15]
	v_cndmask_b32_e64 v70, v70, v160, s[12:13]
	v_cndmask_b32_e64 v69, v69, v160, s[10:11]
	v_cndmask_b32_e64 v68, v68, v160, s[8:9]
	v_cndmask_b32_e64 v67, v67, v160, s[6:7]
	v_cndmask_b32_e32 v66, v66, v160, vcc

.LBB0_249:
	v_mov_b32_e32 v121, v120
	s_add_i32 s1, s68, 0x100
	v_pk_fma_f32 v[154:155], v[66:67], s[84:85], v[120:121] op_sel_hi:[1,0,1]
	v_mul_f32_e32 v67, 0, v179
	s_cmp_lg_u32 0, -1
	v_cndmask_b32_e64 v67, v67, 0, s[4:5]
	s_cselect_b32 s4, 0, 0
	v_add_f32_e32 v66, v114, v115
	s_add_i32 s86, s86, s4
	v_mov_b32_e32 v82, v120
	v_mov_b32_e32 v83, v120
	v_add_f32_e32 v66, v67, v66
	v_add_f32_e32 v180, v116, v117
	s_add_i32 s87, s86, 0x2000
	v_pk_fma_f32 v[140:141], v[80:81], s[84:85], v[82:83] op_sel_hi:[1,0,1]
	v_pk_fma_f32 v[142:143], v[78:79], s[84:85], v[82:83] op_sel_hi:[1,0,1]
	v_pk_fma_f32 v[144:145], v[76:77], s[84:85], v[82:83] op_sel_hi:[1,0,1]
	v_pk_fma_f32 v[146:147], v[74:75], s[84:85], v[82:83] op_sel_hi:[1,0,1]
	v_pk_fma_f32 v[148:149], v[72:73], s[84:85], v[82:83] op_sel_hi:[1,0,1]
	v_pk_fma_f32 v[150:151], v[70:71], s[84:85], v[82:83] op_sel_hi:[1,0,1]
	v_pk_fma_f32 v[152:153], v[68:69], s[84:85], v[82:83] op_sel_hi:[1,0,1]
	v_fmac_f32_e32 v180, v66, v182
	s_cmp_lt_i32 s68, 64
	v_lshl_add_u32 v179, v138, 2, s80
	s_waitcnt vmcnt(0)
	s_barrier
	s_cbranch_scc1 .LBB0_277
	s_add_i32 s6, s77, 0xffffff40
	v_add_u32_e32 v66, s6, v165
	s_lshr_b32 s94, s1, 6
	v_cmp_gt_u32_e64 s[4:5], 32, v163
	v_lshl_add_u32 v182, v165, 2, s80
	v_sub_u32_e32 v183, v66, v138
	s_movk_i32 s95, 0x1bf
	s_mov_b64 s[70:71], 0
	s_mov_b32 s75, 4

.LBB0_257:
	v_cndmask_b32_e64 v120, v116, v139, s[6:7]
	v_mul_f32_e32 v116, 0xbe38aa3b, v120
	v_pk_fma_f32 v[80:81], v[80:81], s[84:85], v[116:117] op_sel_hi:[1,0,0]
	v_pk_fma_f32 v[78:79], v[78:79], s[84:85], v[116:117] op_sel_hi:[1,0,0]
	v_pk_fma_f32 v[76:77], v[76:77], s[84:85], v[116:117] op_sel_hi:[1,0,0]
	v_pk_fma_f32 v[74:75], v[74:75], s[84:85], v[116:117] op_sel_hi:[1,0,0]
	v_pk_fma_f32 v[72:73], v[72:73], s[84:85], v[116:117] op_sel_hi:[1,0,0]
	v_pk_fma_f32 v[70:71], v[70:71], s[84:85], v[116:117] op_sel_hi:[1,0,0]
	v_pk_fma_f32 v[68:69], v[68:69], s[84:85], v[116:117] op_sel_hi:[1,0,0]
	v_pk_fma_f32 v[66:67], v[66:67], s[84:85], v[116:117] op_sel_hi:[1,0,0]
	v_pk_fma_f32 v[154:155], v[88:89], s[84:85], v[116:117] op_sel_hi:[1,0,0]
	v_pk_fma_f32 v[186:187], v[86:87], s[84:85], v[116:117] op_sel_hi:[1,0,0]
	v_pk_fma_f32 v[86:87], v[84:85], s[84:85], v[116:117] op_sel_hi:[1,0,0]
	v_pk_fma_f32 v[88:89], v[82:83], s[84:85], v[116:117] op_sel_hi:[1,0,0]
	v_pk_fma_f32 v[146:147], v[96:97], s[84:85], v[116:117] op_sel_hi:[1,0,0]
	v_pk_fma_f32 v[148:149], v[94:95], s[84:85], v[116:117] op_sel_hi:[1,0,0]
	v_pk_fma_f32 v[150:151], v[92:93], s[84:85], v[116:117] op_sel_hi:[1,0,0]
	v_pk_fma_f32 v[152:153], v[90:91], s[84:85], v[116:117] op_sel_hi:[1,0,0]
	v_exp_f32_e32 v196, v66
	v_exp_f32_e32 v197, v67
	v_exp_f32_e32 v198, v68
	v_exp_f32_e32 v199, v69
	v_exp_f32_e32 v200, v70
	v_exp_f32_e32 v201, v71
	v_exp_f32_e32 v202, v72
	v_exp_f32_e32 v203, v73
	v_exp_f32_e32 v204, v74
	v_exp_f32_e32 v205, v75
	v_exp_f32_e32 v206, v76
	v_exp_f32_e32 v207, v77
	v_exp_f32_e32 v208, v78
	v_exp_f32_e32 v209, v79
	v_exp_f32_e32 v210, v80
	v_exp_f32_e32 v211, v81
	s_waitcnt vmcnt(0)
	s_barrier
	s_add_u32 s6, s72, 0x140000
	s_addc_u32 s7, s73, 0
	s_mov_b32 m0, s81
	s_nop 0
	global_load_lds_dwordx4 v168, s[6:7] offset:0
	s_add_u32 s6, s88, 0x140000
	s_addc_u32 s7, s89, 0
	s_mov_b32 m0, s74
	s_nop 0
	global_load_lds_dwordx4 v169, s[6:7] offset:0
	s_nop 0
	s_mov_b32 m0, s0
	s_nop 0
	global_load_lds_dwordx4 v170, s[6:7] offset:0
	ds_read_b128 v[66:69], v171
	ds_read_b128 v[82:85], v171 offset:4096
	ds_read_b128 v[122:125], v172
	ds_read_b128 v[126:129], v172 offset:4096
	v_exp_f32_e32 v212, v88
	s_waitcnt lgkmcnt(3)
	v_mfma_f32_32x32x16_bf16 v[66:81], v[66:69], v[110:113], 0
	v_exp_f32_e32 v213, v89
	v_exp_f32_e32 v214, v86
	v_exp_f32_e32 v215, v87
	ds_read_b128 v[130:133], v173
	ds_read_b128 v[134:137], v173 offset:4096
	ds_read_b128 v[138:141], v174
	ds_read_b128 v[142:145], v174 offset:4096
	v_exp_f32_e32 v186, v186
	v_exp_f32_e32 v187, v187
	v_exp_f32_e32 v154, v154
	s_waitcnt lgkmcnt(6)
	v_mfma_f32_32x32x16_bf16 v[82:97], v[82:85], v[110:113], 0
	v_exp_f32_e32 v155, v155
	v_exp_f32_e32 v152, v152
	v_exp_f32_e32 v153, v153
	v_exp_f32_e32 v150, v150
	v_exp_f32_e32 v151, v151
	v_exp_f32_e32 v148, v148
	v_exp_f32_e32 v149, v149
	s_waitcnt lgkmcnt(5)
	v_mfma_f32_32x32x16_bf16 v[66:81], v[122:125], v[106:109], v[66:81]
	v_exp_f32_e32 v146, v146
	v_exp_f32_e32 v147, v147
	v_pk_add_f32 v[116:117], v[206:207], v[150:151]
	v_pk_add_f32 v[122:123], v[198:199], v[214:215]
	v_pk_add_f32 v[216:217], v[196:197], v[212:213]
	v_pk_add_f32 v[124:125], v[210:211], v[146:147]
	v_pk_add_f32 v[218:219], v[208:209], v[148:149]
	s_waitcnt lgkmcnt(4)
	v_mfma_f32_32x32x16_bf16 v[82:97], v[126:129], v[106:109], v[82:97]
	v_pk_add_f32 v[126:127], v[202:203], v[154:155]
	v_pk_add_f32 v[128:129], v[204:205], v[152:153]
	v_pk_add_f32 v[220:221], v[200:201], v[186:187]
	v_pk_add_f32 v[128:129], v[216:217], v[128:129]
	v_pk_add_f32 v[218:219], v[220:221], v[218:219]
	v_pk_add_f32 v[124:125], v[126:127], v[124:125]
	v_pk_add_f32 v[116:117], v[122:123], v[116:117]
	s_waitcnt lgkmcnt(3)
	v_mfma_f32_32x32x16_bf16 v[66:81], v[130:133], v[102:105], v[66:81]
	v_pk_add_f32 v[116:117], v[116:117], v[124:125]
	v_pk_add_f32 v[122:123], v[128:129], v[218:219]
	v_pk_add_f32 v[116:117], v[122:123], v[116:117]
	v_cvt_pk_bf16_f32 v122, v196, v197
	v_cvt_pk_bf16_f32 v123, v198, v199
	v_cvt_pk_bf16_f32 v124, v200, v201
	s_waitcnt lgkmcnt(2)
	v_mfma_f32_32x32x16_bf16 v[82:97], v[134:137], v[102:105], v[82:97]
	v_pk_add_f32 v[116:117], v[116:117], v[116:117] op_sel:[0,1] op_sel_hi:[1,0]
	v_cvt_pk_bf16_f32 v125, v202, v203
	v_cvt_pk_bf16_f32 v126, v204, v205
	v_cvt_pk_bf16_f32 v127, v206, v207
	v_cvt_pk_bf16_f32 v128, v208, v209
	v_cvt_pk_bf16_f32 v129, v210, v211
	s_nop 0
	v_mov_b32_e32 v117, v116
	s_waitcnt lgkmcnt(1)
	v_mfma_f32_32x32x16_bf16 v[66:81], v[138:141], v[98:101], v[66:81]
	v_permlane32_swap_b32_e32 v116, v117
	v_cvt_pk_bf16_f32 v130, v212, v213
	v_cvt_pk_bf16_f32 v131, v214, v215
	v_cvt_pk_bf16_f32 v132, v186, v187
	v_cvt_pk_bf16_f32 v133, v154, v155
	v_cvt_pk_bf16_f32 v134, v152, v153
	s_waitcnt lgkmcnt(0)
	v_mfma_f32_32x32x16_bf16 v[82:97], v[142:145], v[98:101], v[82:97]
	v_cvt_pk_bf16_f32 v135, v150, v151
	v_cvt_pk_bf16_f32 v136, v148, v149
	v_cvt_pk_bf16_f32 v137, v146, v147
	v_permlane32_swap_b32_e32 v122, v124
	v_permlane32_swap_b32_e32 v123, v125
	v_permlane32_swap_b32_e32 v126, v128
	v_permlane32_swap_b32_e32 v127, v129
	v_permlane32_swap_b32_e32 v130, v132
	v_permlane32_swap_b32_e32 v131, v133
	v_permlane32_swap_b32_e32 v134, v136
	v_permlane32_swap_b32_e32 v135, v137
	ds_read_b64_tr_b16 v[138:139], v166 offset:0xc000
	ds_read_b64_tr_b16 v[140:141], v166 offset:0xc800
	ds_read_b64_tr_b16 v[142:143], v166 offset:0xd000
	ds_read_b64_tr_b16 v[144:145], v166 offset:0xd800
	ds_read_b64_tr_b16 v[146:147], v166 offset:0xe000
	ds_read_b64_tr_b16 v[148:149], v166 offset:0xe800
	ds_read_b64_tr_b16 v[150:151], v166 offset:0xf000
	ds_read_b64_tr_b16 v[152:153], v166 offset:0xf800
	ds_read_b64_tr_b16 v[196:197], v166 offset:0xc200
	ds_read_b64_tr_b16 v[198:199], v166 offset:0xca00
	ds_read_b64_tr_b16 v[200:201], v166 offset:0xd200
	ds_read_b64_tr_b16 v[202:203], v166 offset:0xda00
	ds_read_b64_tr_b16 v[204:205], v166 offset:0xe200
	ds_read_b64_tr_b16 v[206:207], v166 offset:0xea00
	ds_read_b64_tr_b16 v[208:209], v166 offset:0xf200
	ds_read_b64_tr_b16 v[210:211], v166 offset:0xfa00
	s_waitcnt lgkmcnt(8)
	s_nop 0
	v_mfma_f32_32x32x16_bf16 v[18:33], v[122:125], v[138:141], v[18:33]
	v_mfma_f32_32x32x16_bf16 v[18:33], v[126:129], v[142:145], v[18:33]
	v_mfma_f32_32x32x16_bf16 v[18:33], v[130:133], v[146:149], v[18:33]
	v_mfma_f32_32x32x16_bf16 v[18:33], v[134:137], v[150:153], v[18:33]
	ds_read_b64_tr_b16 v[138:139], v166 offset:0xc400
	ds_read_b64_tr_b16 v[140:141], v166 offset:0xcc00
	ds_read_b64_tr_b16 v[142:143], v166 offset:0xd400
	ds_read_b64_tr_b16 v[144:145], v166 offset:0xdc00
	ds_read_b64_tr_b16 v[146:147], v166 offset:0xe400
	ds_read_b64_tr_b16 v[148:149], v166 offset:0xec00
	ds_read_b64_tr_b16 v[150:151], v166 offset:0xf400
	ds_read_b64_tr_b16 v[152:153], v166 offset:0xfc00
	s_waitcnt lgkmcnt(8)
	v_mfma_f32_32x32x16_bf16 v[34:49], v[122:125], v[196:199], v[34:49]
	v_mfma_f32_32x32x16_bf16 v[34:49], v[126:129], v[200:203], v[34:49]
	v_mfma_f32_32x32x16_bf16 v[34:49], v[130:133], v[204:207], v[34:49]
	v_mfma_f32_32x32x16_bf16 v[34:49], v[134:137], v[208:211], v[34:49]
	ds_read_b64_tr_b16 v[196:197], v166 offset:0xc600
	ds_read_b64_tr_b16 v[198:199], v166 offset:0xce00
	ds_read_b64_tr_b16 v[200:201], v166 offset:0xd600
	ds_read_b64_tr_b16 v[202:203], v166 offset:0xde00
	ds_read_b64_tr_b16 v[204:205], v166 offset:0xe600
	ds_read_b64_tr_b16 v[206:207], v166 offset:0xee00
	ds_read_b64_tr_b16 v[208:209], v166 offset:0xf600
	ds_read_b64_tr_b16 v[210:211], v166 offset:0xfe00
	s_waitcnt lgkmcnt(8)
	v_mfma_f32_32x32x16_bf16 v[50:65], v[122:125], v[138:141], v[50:65]
	v_mfma_f32_32x32x16_bf16 v[50:65], v[126:129], v[142:145], v[50:65]
	v_mfma_f32_32x32x16_bf16 v[50:65], v[130:133], v[146:149], v[50:65]
	v_mfma_f32_32x32x16_bf16 v[50:65], v[134:137], v[150:153], v[50:65]
	s_waitcnt lgkmcnt(0)
	v_mfma_f32_32x32x16_bf16 v[2:17], v[122:125], v[196:199], v[2:17]
	s_add_i32 s6, s95, 0xffffff80
	s_cmp_le_i32 s6, s77
	v_mfma_f32_32x32x16_bf16 v[2:17], v[126:129], v[200:203], v[2:17]
	v_mfma_f32_32x32x16_bf16 v[2:17], v[130:133], v[204:207], v[2:17]
	v_mfma_f32_32x32x16_bf16 v[2:17], v[134:137], v[208:211], v[2:17]
	s_cbranch_scc1 .LBB0_259
	v_subrev_u32_e32 v121, 64, v183
	v_cmp_gt_i32_e64 s[66:67], 26, v121
	v_cmp_gt_i32_e64 s[68:69], 27, v121
	v_cmp_gt_i32_e64 s[64:65], 25, v121
	s_and_b64 s[66:67], s[68:69], s[66:67]
	v_cmp_gt_i32_e64 s[62:63], 24, v121
	s_and_b64 s[64:65], s[66:67], s[64:65]
	v_cmp_gt_i32_e64 s[60:61], 19, v121
	s_and_b64 s[62:63], s[64:65], s[62:63]
	v_cmp_gt_i32_e64 s[58:59], 18, v121
	s_and_b64 s[60:61], s[62:63], s[60:61]
	v_cmp_gt_i32_e64 s[56:57], 17, v121
	s_and_b64 s[58:59], s[60:61], s[58:59]
	v_cmp_gt_i32_e64 s[54:55], 16, v121
	s_and_b64 s[56:57], s[58:59], s[56:57]
	v_cmp_gt_i32_e64 s[52:53], 11, v121
	s_and_b64 s[54:55], s[56:57], s[54:55]
	v_cmp_gt_i32_e64 s[50:51], 10, v121
	s_and_b64 s[52:53], s[54:55], s[52:53]
	v_cmp_gt_i32_e64 s[48:49], 9, v121
	s_and_b64 s[50:51], s[52:53], s[50:51]
	v_cmp_gt_i32_e64 s[44:45], 8, v121
	s_and_b64 s[48:49], s[50:51], s[48:49]
	v_cmp_gt_i32_e64 s[42:43], 3, v121
	s_and_b64 s[44:45], s[48:49], s[44:45]
	v_cmp_gt_i32_e64 s[40:41], 2, v121
	s_and_b64 s[42:43], s[44:45], s[42:43]
	v_cmp_gt_i32_e64 s[38:39], 1, v121
	s_and_b64 s[40:41], s[42:43], s[40:41]
	v_cmp_gt_i32_e64 s[36:37], 0, v121
	s_and_b64 s[38:39], s[40:41], s[38:39]
	s_and_b64 s[36:37], s[38:39], s[36:37]
	v_cmp_gt_i32_e64 s[34:35], 58, v121
	v_cndmask_b32_e64 v66, v66, v160, s[36:37]
	v_cmp_gt_i32_e64 s[36:37], 59, v121
	v_cmp_gt_i32_e64 s[30:31], 57, v121
	s_and_b64 s[34:35], s[36:37], s[34:35]
	v_cmp_gt_i32_e64 s[28:29], 56, v121
	s_and_b64 s[30:31], s[34:35], s[30:31]
	v_cmp_gt_i32_e64 s[26:27], 51, v121
	s_and_b64 s[28:29], s[30:31], s[28:29]
	v_cmp_gt_i32_e64 s[24:25], 50, v121
	s_and_b64 s[26:27], s[28:29], s[26:27]
	v_cmp_gt_i32_e64 s[22:23], 49, v121
	s_and_b64 s[24:25], s[26:27], s[24:25]
	v_cmp_gt_i32_e64 s[20:21], 48, v121
	s_and_b64 s[22:23], s[24:25], s[22:23]
	v_cmp_gt_i32_e64 s[18:19], 43, v121
	s_and_b64 s[20:21], s[22:23], s[20:21]
	v_cmp_gt_i32_e64 s[16:17], 42, v121
	s_and_b64 s[18:19], s[20:21], s[18:19]
	v_cmp_gt_i32_e64 s[14:15], 41, v121
	s_and_b64 s[16:17], s[18:19], s[16:17]
	v_cmp_gt_i32_e64 s[12:13], 40, v121
	s_and_b64 s[14:15], s[16:17], s[14:15]
	v_cmp_gt_i32_e64 s[10:11], 35, v121
	s_and_b64 s[12:13], s[14:15], s[12:13]
	v_cmp_gt_i32_e64 s[8:9], 34, v121
	s_and_b64 s[10:11], s[12:13], s[10:11]
	v_cmp_gt_i32_e64 s[6:7], 33, v121
	s_and_b64 s[8:9], s[10:11], s[8:9]
	v_cmp_gt_i32_e32 vcc, 32, v121
	s_and_b64 s[6:7], s[8:9], s[6:7]
	s_and_b64 vcc, s[6:7], vcc
	v_cndmask_b32_e64 v81, v81, v160, s[68:69]
	v_cndmask_b32_e64 v80, v80, v160, s[66:67]
	v_cndmask_b32_e64 v79, v79, v160, s[64:65]
	v_cndmask_b32_e64 v78, v78, v160, s[62:63]
	v_cndmask_b32_e64 v77, v77, v160, s[60:61]
	v_cndmask_b32_e64 v76, v76, v160, s[58:59]
	v_cndmask_b32_e64 v75, v75, v160, s[56:57]
	v_cndmask_b32_e64 v74, v74, v160, s[54:55]
	v_cndmask_b32_e64 v73, v73, v160, s[52:53]
	v_cndmask_b32_e64 v72, v72, v160, s[50:51]
	v_cndmask_b32_e64 v71, v71, v160, s[48:49]
	v_cndmask_b32_e64 v70, v70, v160, s[44:45]
	v_cndmask_b32_e64 v69, v69, v160, s[42:43]
	v_cndmask_b32_e64 v68, v68, v160, s[40:41]
	v_cndmask_b32_e64 v67, v67, v160, s[38:39]
	v_cndmask_b32_e64 v97, v97, v160, s[36:37]
	v_cndmask_b32_e64 v96, v96, v160, s[34:35]
	v_cndmask_b32_e64 v95, v95, v160, s[30:31]
	v_cndmask_b32_e64 v94, v94, v160, s[28:29]
	v_cndmask_b32_e64 v93, v93, v160, s[26:27]
	v_cndmask_b32_e64 v92, v92, v160, s[24:25]
	v_cndmask_b32_e64 v91, v91, v160, s[22:23]
	v_cndmask_b32_e64 v90, v90, v160, s[20:21]
	v_cndmask_b32_e64 v89, v89, v160, s[18:19]
	v_cndmask_b32_e64 v88, v88, v160, s[16:17]
	v_cndmask_b32_e64 v87, v87, v160, s[14:15]
	v_cndmask_b32_e64 v86, v86, v160, s[12:13]
	v_cndmask_b32_e64 v85, v85, v160, s[10:11]
	v_cndmask_b32_e64 v84, v84, v160, s[8:9]
	v_cndmask_b32_e64 v83, v83, v160, s[6:7]
	v_cndmask_b32_e32 v82, v82, v160, vcc

.LBB0_263:
	v_cndmask_b32_e64 v122, v121, v120, s[6:7]
	v_mul_f32_e32 v120, 0xbe38aa3b, v122
	v_pk_fma_f32 v[80:81], v[80:81], s[84:85], v[120:121] op_sel_hi:[1,0,0]
	v_pk_fma_f32 v[78:79], v[78:79], s[84:85], v[120:121] op_sel_hi:[1,0,0]
	v_pk_fma_f32 v[76:77], v[76:77], s[84:85], v[120:121] op_sel_hi:[1,0,0]
	v_pk_fma_f32 v[74:75], v[74:75], s[84:85], v[120:121] op_sel_hi:[1,0,0]
	v_pk_fma_f32 v[72:73], v[72:73], s[84:85], v[120:121] op_sel_hi:[1,0,0]
	v_pk_fma_f32 v[70:71], v[70:71], s[84:85], v[120:121] op_sel_hi:[1,0,0]
	v_pk_fma_f32 v[68:69], v[68:69], s[84:85], v[120:121] op_sel_hi:[1,0,0]
	v_pk_fma_f32 v[66:67], v[66:67], s[84:85], v[120:121] op_sel_hi:[1,0,0]
	v_pk_fma_f32 v[186:187], v[88:89], s[84:85], v[120:121] op_sel_hi:[1,0,0]
	v_pk_fma_f32 v[196:197], v[86:87], s[84:85], v[120:121] op_sel_hi:[1,0,0]
	v_pk_fma_f32 v[86:87], v[84:85], s[84:85], v[120:121] op_sel_hi:[1,0,0]
	v_pk_fma_f32 v[88:89], v[82:83], s[84:85], v[120:121] op_sel_hi:[1,0,0]
	v_pk_fma_f32 v[148:149], v[96:97], s[84:85], v[120:121] op_sel_hi:[1,0,0]
	v_pk_fma_f32 v[150:151], v[94:95], s[84:85], v[120:121] op_sel_hi:[1,0,0]
	v_pk_fma_f32 v[152:153], v[92:93], s[84:85], v[120:121] op_sel_hi:[1,0,0]
	v_pk_fma_f32 v[154:155], v[90:91], s[84:85], v[120:121] op_sel_hi:[1,0,0]
	v_exp_f32_e32 v198, v66
	v_exp_f32_e32 v199, v67
	v_exp_f32_e32 v200, v68
	v_exp_f32_e32 v201, v69
	v_exp_f32_e32 v202, v70
	v_exp_f32_e32 v203, v71
	v_exp_f32_e32 v204, v72
	v_exp_f32_e32 v205, v73
	v_exp_f32_e32 v206, v74
	v_exp_f32_e32 v207, v75
	v_exp_f32_e32 v208, v76
	v_exp_f32_e32 v209, v77
	v_exp_f32_e32 v210, v78
	v_exp_f32_e32 v211, v79
	v_exp_f32_e32 v212, v80
	v_exp_f32_e32 v213, v81
	s_waitcnt vmcnt(0)
	s_barrier
	s_add_u32 s6, s72, 0x180000
	s_addc_u32 s7, s73, 0
	s_mov_b32 m0, s85
	s_nop 0
	global_load_lds_dwordx4 v168, s[6:7] offset:0
	s_add_u32 s6, s88, 0x180000
	s_addc_u32 s7, s89, 0
	s_mov_b32 m0, s82
	s_nop 0
	global_load_lds_dwordx4 v169, s[6:7] offset:0
	s_nop 0
	s_mov_b32 m0, s83
	s_nop 0
	global_load_lds_dwordx4 v170, s[6:7] offset:0
	ds_read_b128 v[66:69], v175
	ds_read_b128 v[82:85], v175 offset:4096
	ds_read_b128 v[124:127], v176
	ds_read_b128 v[128:131], v176 offset:4096
	v_exp_f32_e32 v214, v88
	s_waitcnt lgkmcnt(3)
	v_mfma_f32_32x32x16_bf16 v[66:81], v[66:69], v[110:113], 0
	v_exp_f32_e32 v215, v89
	v_exp_f32_e32 v216, v86
	v_exp_f32_e32 v217, v87
	ds_read_b128 v[132:135], v177
	ds_read_b128 v[136:139], v177 offset:4096
	ds_read_b128 v[140:143], v178
	ds_read_b128 v[144:147], v178 offset:4096
	v_exp_f32_e32 v196, v196
	v_exp_f32_e32 v197, v197
	v_exp_f32_e32 v218, v186
	s_waitcnt lgkmcnt(6)
	v_mfma_f32_32x32x16_bf16 v[82:97], v[82:85], v[110:113], 0
	v_exp_f32_e32 v219, v187
	v_exp_f32_e32 v154, v154
	v_exp_f32_e32 v155, v155
	v_exp_f32_e32 v152, v152
	v_exp_f32_e32 v153, v153
	v_exp_f32_e32 v150, v150
	v_exp_f32_e32 v151, v151
	s_waitcnt lgkmcnt(5)
	v_mfma_f32_32x32x16_bf16 v[66:81], v[124:127], v[106:109], v[66:81]
	v_exp_f32_e32 v148, v148
	v_exp_f32_e32 v149, v149
	v_pk_add_f32 v[120:121], v[208:209], v[152:153]
	v_pk_add_f32 v[124:125], v[200:201], v[216:217]
	v_pk_add_f32 v[186:187], v[198:199], v[214:215]
	v_pk_add_f32 v[126:127], v[212:213], v[148:149]
	v_pk_add_f32 v[220:221], v[210:211], v[150:151]
	s_waitcnt lgkmcnt(4)
	v_mfma_f32_32x32x16_bf16 v[82:97], v[128:131], v[106:109], v[82:97]
	v_pk_add_f32 v[128:129], v[204:205], v[218:219]
	v_pk_add_f32 v[130:131], v[206:207], v[154:155]
	v_pk_add_f32 v[222:223], v[202:203], v[196:197]
	v_pk_add_f32 v[130:131], v[186:187], v[130:131]
	v_pk_add_f32 v[220:221], v[222:223], v[220:221]
	v_pk_add_f32 v[126:127], v[128:129], v[126:127]
	v_pk_add_f32 v[120:121], v[124:125], v[120:121]
	s_waitcnt lgkmcnt(3)
	v_mfma_f32_32x32x16_bf16 v[66:81], v[132:135], v[102:105], v[66:81]
	v_pk_add_f32 v[120:121], v[120:121], v[126:127]
	v_pk_add_f32 v[124:125], v[130:131], v[220:221]
	v_pk_add_f32 v[120:121], v[124:125], v[120:121]
	v_cvt_pk_bf16_f32 v124, v198, v199
	v_cvt_pk_bf16_f32 v125, v200, v201
	v_cvt_pk_bf16_f32 v126, v202, v203
	s_waitcnt lgkmcnt(2)
	v_mfma_f32_32x32x16_bf16 v[82:97], v[136:139], v[102:105], v[82:97]
	v_pk_add_f32 v[120:121], v[120:121], v[120:121] op_sel:[0,1] op_sel_hi:[1,0]
	v_cvt_pk_bf16_f32 v127, v204, v205
	v_cvt_pk_bf16_f32 v128, v206, v207
	v_cvt_pk_bf16_f32 v129, v208, v209
	v_cvt_pk_bf16_f32 v130, v210, v211
	v_cvt_pk_bf16_f32 v131, v212, v213
	s_nop 0
	v_mov_b32_e32 v186, v120
	s_waitcnt lgkmcnt(1)
	v_mfma_f32_32x32x16_bf16 v[66:81], v[140:143], v[98:101], v[66:81]
	v_permlane32_swap_b32_e32 v120, v186
	v_cvt_pk_bf16_f32 v132, v214, v215
	v_cvt_pk_bf16_f32 v133, v216, v217
	v_cvt_pk_bf16_f32 v134, v196, v197
	v_cvt_pk_bf16_f32 v135, v218, v219
	v_cvt_pk_bf16_f32 v136, v154, v155
	s_waitcnt lgkmcnt(0)
	v_mfma_f32_32x32x16_bf16 v[82:97], v[144:147], v[98:101], v[82:97]
	v_cvt_pk_bf16_f32 v137, v152, v153
	v_cvt_pk_bf16_f32 v138, v150, v151
	v_cvt_pk_bf16_f32 v139, v148, v149
	v_permlane32_swap_b32_e32 v124, v126
	v_permlane32_swap_b32_e32 v125, v127
	v_permlane32_swap_b32_e32 v128, v130
	v_permlane32_swap_b32_e32 v129, v131
	v_permlane32_swap_b32_e32 v132, v134
	v_permlane32_swap_b32_e32 v133, v135
	v_permlane32_swap_b32_e32 v136, v138
	v_permlane32_swap_b32_e32 v137, v139
	ds_read_b64_tr_b16 v[140:141], v166 offset:0
	ds_read_b64_tr_b16 v[142:143], v166 offset:0x800
	ds_read_b64_tr_b16 v[144:145], v166 offset:0x1000
	ds_read_b64_tr_b16 v[146:147], v166 offset:0x1800
	ds_read_b64_tr_b16 v[148:149], v166 offset:0x2000
	ds_read_b64_tr_b16 v[150:151], v166 offset:0x2800
	ds_read_b64_tr_b16 v[152:153], v166 offset:0x3000
	ds_read_b64_tr_b16 v[154:155], v166 offset:0x3800
	ds_read_b64_tr_b16 v[196:197], v166 offset:0x200
	ds_read_b64_tr_b16 v[198:199], v166 offset:0xa00
	ds_read_b64_tr_b16 v[200:201], v166 offset:0x1200
	ds_read_b64_tr_b16 v[202:203], v166 offset:0x1a00
	ds_read_b64_tr_b16 v[204:205], v166 offset:0x2200
	ds_read_b64_tr_b16 v[206:207], v166 offset:0x2a00
	ds_read_b64_tr_b16 v[208:209], v166 offset:0x3200
	ds_read_b64_tr_b16 v[210:211], v166 offset:0x3a00
	s_waitcnt lgkmcnt(8)
	s_nop 0
	v_mfma_f32_32x32x16_bf16 v[18:33], v[124:127], v[140:143], v[18:33]
	v_mfma_f32_32x32x16_bf16 v[18:33], v[128:131], v[144:147], v[18:33]
	v_mfma_f32_32x32x16_bf16 v[18:33], v[132:135], v[148:151], v[18:33]
	v_mfma_f32_32x32x16_bf16 v[18:33], v[136:139], v[152:155], v[18:33]
	ds_read_b64_tr_b16 v[140:141], v166 offset:0x400
	ds_read_b64_tr_b16 v[142:143], v166 offset:0xc00
	ds_read_b64_tr_b16 v[144:145], v166 offset:0x1400
	ds_read_b64_tr_b16 v[146:147], v166 offset:0x1c00
	ds_read_b64_tr_b16 v[148:149], v166 offset:0x2400
	ds_read_b64_tr_b16 v[150:151], v166 offset:0x2c00
	ds_read_b64_tr_b16 v[152:153], v166 offset:0x3400
	ds_read_b64_tr_b16 v[154:155], v166 offset:0x3c00
	s_waitcnt lgkmcnt(8)
	v_mfma_f32_32x32x16_bf16 v[34:49], v[124:127], v[196:199], v[34:49]
	v_mfma_f32_32x32x16_bf16 v[34:49], v[128:131], v[200:203], v[34:49]
	v_mfma_f32_32x32x16_bf16 v[34:49], v[132:135], v[204:207], v[34:49]
	v_mfma_f32_32x32x16_bf16 v[34:49], v[136:139], v[208:211], v[34:49]
	ds_read_b64_tr_b16 v[196:197], v166 offset:0x600
	ds_read_b64_tr_b16 v[198:199], v166 offset:0xe00
	ds_read_b64_tr_b16 v[200:201], v166 offset:0x1600
	ds_read_b64_tr_b16 v[202:203], v166 offset:0x1e00
	ds_read_b64_tr_b16 v[204:205], v166 offset:0x2600
	ds_read_b64_tr_b16 v[206:207], v166 offset:0x2e00
	ds_read_b64_tr_b16 v[208:209], v166 offset:0x3600
	ds_read_b64_tr_b16 v[210:211], v166 offset:0x3e00
	s_waitcnt lgkmcnt(8)
	v_mfma_f32_32x32x16_bf16 v[50:65], v[124:127], v[140:143], v[50:65]
	v_mfma_f32_32x32x16_bf16 v[50:65], v[128:131], v[144:147], v[50:65]
	v_mfma_f32_32x32x16_bf16 v[50:65], v[132:135], v[148:151], v[50:65]
	v_mfma_f32_32x32x16_bf16 v[50:65], v[136:139], v[152:155], v[50:65]
	s_waitcnt lgkmcnt(0)
	v_mfma_f32_32x32x16_bf16 v[2:17], v[124:127], v[196:199], v[2:17]
	s_sub_i32 s6, s95, 64
	s_cmp_le_i32 s6, s77
	v_mfma_f32_32x32x16_bf16 v[2:17], v[128:131], v[200:203], v[2:17]
	v_mfma_f32_32x32x16_bf16 v[2:17], v[132:135], v[204:207], v[2:17]
	v_mfma_f32_32x32x16_bf16 v[2:17], v[136:139], v[208:211], v[2:17]
	s_cbranch_scc1 .LBB0_265
	v_add_u32_e32 v121, 0xffffff80, v183
	v_cmp_gt_i32_e64 s[66:67], 26, v121
	v_cmp_gt_i32_e64 s[68:69], 27, v121
	v_cmp_gt_i32_e64 s[64:65], 25, v121
	s_and_b64 s[66:67], s[68:69], s[66:67]
	v_cmp_gt_i32_e64 s[62:63], 24, v121
	s_and_b64 s[64:65], s[66:67], s[64:65]
	v_cmp_gt_i32_e64 s[60:61], 19, v121
	s_and_b64 s[62:63], s[64:65], s[62:63]
	v_cmp_gt_i32_e64 s[58:59], 18, v121
	s_and_b64 s[60:61], s[62:63], s[60:61]
	v_cmp_gt_i32_e64 s[56:57], 17, v121
	s_and_b64 s[58:59], s[60:61], s[58:59]
	v_cmp_gt_i32_e64 s[54:55], 16, v121
	s_and_b64 s[56:57], s[58:59], s[56:57]
	v_cmp_gt_i32_e64 s[52:53], 11, v121
	s_and_b64 s[54:55], s[56:57], s[54:55]
	v_cmp_gt_i32_e64 s[50:51], 10, v121
	s_and_b64 s[52:53], s[54:55], s[52:53]
	v_cmp_gt_i32_e64 s[48:49], 9, v121
	s_and_b64 s[50:51], s[52:53], s[50:51]
	v_cmp_gt_i32_e64 s[44:45], 8, v121
	s_and_b64 s[48:49], s[50:51], s[48:49]
	v_cmp_gt_i32_e64 s[42:43], 3, v121
	s_and_b64 s[44:45], s[48:49], s[44:45]
	v_cmp_gt_i32_e64 s[40:41], 2, v121
	s_and_b64 s[42:43], s[44:45], s[42:43]
	v_cmp_gt_i32_e64 s[38:39], 1, v121
	s_and_b64 s[40:41], s[42:43], s[40:41]
	v_cmp_gt_i32_e64 s[36:37], 0, v121
	s_and_b64 s[38:39], s[40:41], s[38:39]
	s_and_b64 s[36:37], s[38:39], s[36:37]
	v_cmp_gt_i32_e64 s[34:35], 58, v121
	v_cndmask_b32_e64 v66, v66, v160, s[36:37]
	v_cmp_gt_i32_e64 s[36:37], 59, v121
	v_cmp_gt_i32_e64 s[30:31], 57, v121
	s_and_b64 s[34:35], s[36:37], s[34:35]
	v_cmp_gt_i32_e64 s[28:29], 56, v121
	s_and_b64 s[30:31], s[34:35], s[30:31]
	v_cmp_gt_i32_e64 s[26:27], 51, v121
	s_and_b64 s[28:29], s[30:31], s[28:29]
	v_cmp_gt_i32_e64 s[24:25], 50, v121
	s_and_b64 s[26:27], s[28:29], s[26:27]
	v_cmp_gt_i32_e64 s[22:23], 49, v121
	s_and_b64 s[24:25], s[26:27], s[24:25]
	v_cmp_gt_i32_e64 s[20:21], 48, v121
	s_and_b64 s[22:23], s[24:25], s[22:23]
	v_cmp_gt_i32_e64 s[18:19], 43, v121
	s_and_b64 s[20:21], s[22:23], s[20:21]
	v_cmp_gt_i32_e64 s[16:17], 42, v121
	s_and_b64 s[18:19], s[20:21], s[18:19]
	v_cmp_gt_i32_e64 s[14:15], 41, v121
	s_and_b64 s[16:17], s[18:19], s[16:17]
	v_cmp_gt_i32_e64 s[12:13], 40, v121
	s_and_b64 s[14:15], s[16:17], s[14:15]
	v_cmp_gt_i32_e64 s[10:11], 35, v121
	s_and_b64 s[12:13], s[14:15], s[12:13]
	v_cmp_gt_i32_e64 s[8:9], 34, v121
	s_and_b64 s[10:11], s[12:13], s[10:11]
	v_cmp_gt_i32_e64 s[6:7], 33, v121
	s_and_b64 s[8:9], s[10:11], s[8:9]
	v_cmp_gt_i32_e32 vcc, 32, v121
	s_and_b64 s[6:7], s[8:9], s[6:7]
	s_and_b64 vcc, s[6:7], vcc
	v_cndmask_b32_e64 v81, v81, v160, s[68:69]
	v_cndmask_b32_e64 v80, v80, v160, s[66:67]
	v_cndmask_b32_e64 v79, v79, v160, s[64:65]
	v_cndmask_b32_e64 v78, v78, v160, s[62:63]
	v_cndmask_b32_e64 v77, v77, v160, s[60:61]
	v_cndmask_b32_e64 v76, v76, v160, s[58:59]
	v_cndmask_b32_e64 v75, v75, v160, s[56:57]
	v_cndmask_b32_e64 v74, v74, v160, s[54:55]
	v_cndmask_b32_e64 v73, v73, v160, s[52:53]
	v_cndmask_b32_e64 v72, v72, v160, s[50:51]
	v_cndmask_b32_e64 v71, v71, v160, s[48:49]
	v_cndmask_b32_e64 v70, v70, v160, s[44:45]
	v_cndmask_b32_e64 v69, v69, v160, s[42:43]
	v_cndmask_b32_e64 v68, v68, v160, s[40:41]
	v_cndmask_b32_e64 v67, v67, v160, s[38:39]
	v_cndmask_b32_e64 v97, v97, v160, s[36:37]
	v_cndmask_b32_e64 v96, v96, v160, s[34:35]
	v_cndmask_b32_e64 v95, v95, v160, s[30:31]
	v_cndmask_b32_e64 v94, v94, v160, s[28:29]
	v_cndmask_b32_e64 v93, v93, v160, s[26:27]
	v_cndmask_b32_e64 v92, v92, v160, s[24:25]
	v_cndmask_b32_e64 v91, v91, v160, s[22:23]
	v_cndmask_b32_e64 v90, v90, v160, s[20:21]
	v_cndmask_b32_e64 v89, v89, v160, s[18:19]
	v_cndmask_b32_e64 v88, v88, v160, s[16:17]
	v_cndmask_b32_e64 v87, v87, v160, s[14:15]
	v_cndmask_b32_e64 v86, v86, v160, s[12:13]
	v_cndmask_b32_e64 v85, v85, v160, s[10:11]
	v_cndmask_b32_e64 v84, v84, v160, s[8:9]
	v_cndmask_b32_e64 v83, v83, v160, s[6:7]
	v_cndmask_b32_e32 v82, v82, v160, vcc

.LBB0_269:
	v_cndmask_b32_e64 v121, v121, v122, s[6:7]
	v_mul_f32_e32 v122, 0xbe38aa3b, v121
	v_pk_fma_f32 v[80:81], v[80:81], s[84:85], v[122:123] op_sel_hi:[1,0,0]
	v_pk_fma_f32 v[78:79], v[78:79], s[84:85], v[122:123] op_sel_hi:[1,0,0]
	v_pk_fma_f32 v[76:77], v[76:77], s[84:85], v[122:123] op_sel_hi:[1,0,0]
	v_pk_fma_f32 v[74:75], v[74:75], s[84:85], v[122:123] op_sel_hi:[1,0,0]
	v_pk_fma_f32 v[72:73], v[72:73], s[84:85], v[122:123] op_sel_hi:[1,0,0]
	v_pk_fma_f32 v[70:71], v[70:71], s[84:85], v[122:123] op_sel_hi:[1,0,0]
	v_pk_fma_f32 v[68:69], v[68:69], s[84:85], v[122:123] op_sel_hi:[1,0,0]
	v_pk_fma_f32 v[66:67], v[66:67], s[84:85], v[122:123] op_sel_hi:[1,0,0]
	v_pk_fma_f32 v[138:139], v[96:97], s[84:85], v[122:123] op_sel_hi:[1,0,0]
	v_pk_fma_f32 v[148:149], v[94:95], s[84:85], v[122:123] op_sel_hi:[1,0,0]
	v_pk_fma_f32 v[150:151], v[92:93], s[84:85], v[122:123] op_sel_hi:[1,0,0]
	v_pk_fma_f32 v[152:153], v[90:91], s[84:85], v[122:123] op_sel_hi:[1,0,0]
	v_pk_fma_f32 v[154:155], v[88:89], s[84:85], v[122:123] op_sel_hi:[1,0,0]
	v_pk_fma_f32 v[196:197], v[86:87], s[84:85], v[122:123] op_sel_hi:[1,0,0]
	v_pk_fma_f32 v[198:199], v[84:85], s[84:85], v[122:123] op_sel_hi:[1,0,0]
	v_pk_fma_f32 v[200:201], v[82:83], s[84:85], v[122:123] op_sel_hi:[1,0,0]
	v_exp_f32_e32 v202, v66
	v_exp_f32_e32 v203, v67
	v_exp_f32_e32 v204, v68
	v_exp_f32_e32 v205, v69
	v_exp_f32_e32 v206, v70
	v_exp_f32_e32 v207, v71
	v_exp_f32_e32 v208, v72
	v_exp_f32_e32 v209, v73
	v_exp_f32_e32 v210, v74
	v_exp_f32_e32 v211, v75
	v_exp_f32_e32 v212, v76
	v_exp_f32_e32 v213, v77
	v_exp_f32_e32 v214, v78
	v_exp_f32_e32 v215, v79
	v_exp_f32_e32 v216, v80
	v_exp_f32_e32 v217, v81
	s_waitcnt vmcnt(0)
	s_barrier
	s_add_u32 s6, s72, 0x1c0000
	s_addc_u32 s7, s73, 0
	s_mov_b32 m0, s81
	s_nop 0
	global_load_lds_dwordx4 v168, s[6:7] offset:0
	s_add_u32 s6, s88, 0x1c0000
	s_addc_u32 s7, s89, 0
	s_mov_b32 m0, s78
	s_nop 0
	global_load_lds_dwordx4 v169, s[6:7] offset:0
	s_nop 0
	s_mov_b32 m0, s79
	s_nop 0
	global_load_lds_dwordx4 v170, s[6:7] offset:0
	ds_read_b128 v[66:69], v171
	ds_read_b128 v[70:73], v171 offset:4096
	ds_read_b128 v[122:125], v172
	ds_read_b128 v[126:129], v172 offset:4096
	ds_read_b128 v[130:133], v173
	ds_read_b128 v[134:137], v173 offset:4096
	ds_read_b128 v[140:143], v174
	ds_read_b128 v[144:147], v174 offset:4096
	s_waitcnt lgkmcnt(7)
	v_mfma_f32_32x32x16_bf16 v[82:97], v[66:69], v[110:113], 0
	v_exp_f32_e32 v200, v200
	v_exp_f32_e32 v201, v201
	v_exp_f32_e32 v198, v198
	v_exp_f32_e32 v199, v199
	v_exp_f32_e32 v196, v196
	v_exp_f32_e32 v197, v197
	v_exp_f32_e32 v154, v154
	s_waitcnt lgkmcnt(6)
	v_mfma_f32_32x32x16_bf16 v[66:81], v[70:73], v[110:113], 0
	v_exp_f32_e32 v155, v155
	v_exp_f32_e32 v152, v152
	v_exp_f32_e32 v153, v153
	v_exp_f32_e32 v150, v150
	v_exp_f32_e32 v151, v151
	v_exp_f32_e32 v148, v148
	v_exp_f32_e32 v149, v149
	s_waitcnt lgkmcnt(5)
	v_mfma_f32_32x32x16_bf16 v[82:97], v[122:125], v[106:109], v[82:97]
	v_exp_f32_e32 v218, v138
	v_exp_f32_e32 v219, v139
	v_pk_add_f32 v[122:123], v[212:213], v[150:151]
	v_pk_add_f32 v[124:125], v[204:205], v[198:199]
	v_pk_add_f32 v[138:139], v[210:211], v[152:153]
	v_pk_add_f32 v[220:221], v[202:203], v[200:201]
	v_pk_add_f32 v[222:223], v[214:215], v[148:149]
	s_waitcnt lgkmcnt(4)
	v_mfma_f32_32x32x16_bf16 v[66:81], v[126:129], v[106:109], v[66:81]
	v_pk_add_f32 v[126:127], v[216:217], v[218:219]
	v_pk_add_f32 v[128:129], v[208:209], v[154:155]
	v_pk_add_f32 v[224:225], v[206:207], v[196:197]
	v_pk_add_f32 v[126:127], v[128:129], v[126:127]
	v_pk_add_f32 v[222:223], v[224:225], v[222:223]
	v_pk_add_f32 v[122:123], v[124:125], v[122:123]
	s_waitcnt lgkmcnt(3)
	v_mfma_f32_32x32x16_bf16 v[82:97], v[130:133], v[102:105], v[82:97]
	v_pk_add_f32 v[130:131], v[220:221], v[138:139]
	v_pk_add_f32 v[122:123], v[122:123], v[126:127]
	v_pk_add_f32 v[124:125], v[130:131], v[222:223]
	v_pk_add_f32 v[122:123], v[124:125], v[122:123]
	s_nop 0
	v_pk_add_f32 v[138:139], v[122:123], v[122:123] op_sel:[0,1] op_sel_hi:[1,0]
	s_waitcnt lgkmcnt(2)
	v_mfma_f32_32x32x16_bf16 v[66:81], v[134:137], v[102:105], v[66:81]
	v_mov_b32_e32 v195, v138
	s_nop 1
	v_permlane32_swap_b32_e32 v138, v195
	v_cvt_pk_bf16_f32 v122, v202, v203
	v_cvt_pk_bf16_f32 v123, v204, v205
	v_cvt_pk_bf16_f32 v124, v206, v207
	v_cvt_pk_bf16_f32 v125, v208, v209
	s_waitcnt lgkmcnt(1)
	v_mfma_f32_32x32x16_bf16 v[82:97], v[140:143], v[98:101], v[82:97]
	v_cvt_pk_bf16_f32 v126, v210, v211
	v_cvt_pk_bf16_f32 v127, v212, v213
	v_cvt_pk_bf16_f32 v128, v214, v215
	v_cvt_pk_bf16_f32 v129, v216, v217
	v_cvt_pk_bf16_f32 v130, v200, v201
	v_cvt_pk_bf16_f32 v131, v198, v199
	v_cvt_pk_bf16_f32 v132, v196, v197
	s_waitcnt lgkmcnt(0)
	v_mfma_f32_32x32x16_bf16 v[66:81], v[144:147], v[98:101], v[66:81]
	v_cvt_pk_bf16_f32 v133, v154, v155
	v_cvt_pk_bf16_f32 v134, v152, v153
	v_cvt_pk_bf16_f32 v135, v150, v151
	v_cvt_pk_bf16_f32 v136, v148, v149
	v_cvt_pk_bf16_f32 v137, v218, v219
	v_permlane32_swap_b32_e32 v122, v124
	v_permlane32_swap_b32_e32 v123, v125
	v_permlane32_swap_b32_e32 v126, v128
	v_permlane32_swap_b32_e32 v127, v129
	v_permlane32_swap_b32_e32 v130, v132
	v_permlane32_swap_b32_e32 v131, v133
	v_permlane32_swap_b32_e32 v134, v136
	v_permlane32_swap_b32_e32 v135, v137
	ds_read_b64_tr_b16 v[140:141], v166 offset:0x4000
	ds_read_b64_tr_b16 v[142:143], v166 offset:0x4800
	ds_read_b64_tr_b16 v[144:145], v166 offset:0x5000
	ds_read_b64_tr_b16 v[146:147], v166 offset:0x5800
	ds_read_b64_tr_b16 v[148:149], v166 offset:0x6000
	ds_read_b64_tr_b16 v[150:151], v166 offset:0x6800
	ds_read_b64_tr_b16 v[152:153], v166 offset:0x7000
	ds_read_b64_tr_b16 v[154:155], v166 offset:0x7800
	ds_read_b64_tr_b16 v[196:197], v166 offset:0x4200
	ds_read_b64_tr_b16 v[198:199], v166 offset:0x4a00
	ds_read_b64_tr_b16 v[200:201], v166 offset:0x5200
	ds_read_b64_tr_b16 v[202:203], v166 offset:0x5a00
	ds_read_b64_tr_b16 v[204:205], v166 offset:0x6200
	ds_read_b64_tr_b16 v[206:207], v166 offset:0x6a00
	ds_read_b64_tr_b16 v[208:209], v166 offset:0x7200
	ds_read_b64_tr_b16 v[210:211], v166 offset:0x7a00
	s_waitcnt lgkmcnt(8)
	s_nop 0
	v_mfma_f32_32x32x16_bf16 v[18:33], v[122:125], v[140:143], v[18:33]
	v_mfma_f32_32x32x16_bf16 v[18:33], v[126:129], v[144:147], v[18:33]
	v_mfma_f32_32x32x16_bf16 v[18:33], v[130:133], v[148:151], v[18:33]
	v_mfma_f32_32x32x16_bf16 v[18:33], v[134:137], v[152:155], v[18:33]
	ds_read_b64_tr_b16 v[140:141], v166 offset:0x4400
	ds_read_b64_tr_b16 v[142:143], v166 offset:0x4c00
	ds_read_b64_tr_b16 v[144:145], v166 offset:0x5400
	ds_read_b64_tr_b16 v[146:147], v166 offset:0x5c00
	ds_read_b64_tr_b16 v[148:149], v166 offset:0x6400
	ds_read_b64_tr_b16 v[150:151], v166 offset:0x6c00
	ds_read_b64_tr_b16 v[152:153], v166 offset:0x7400
	ds_read_b64_tr_b16 v[154:155], v166 offset:0x7c00
	s_waitcnt lgkmcnt(8)
	v_mfma_f32_32x32x16_bf16 v[34:49], v[122:125], v[196:199], v[34:49]
	v_mfma_f32_32x32x16_bf16 v[34:49], v[126:129], v[200:203], v[34:49]
	v_mfma_f32_32x32x16_bf16 v[34:49], v[130:133], v[204:207], v[34:49]
	v_mfma_f32_32x32x16_bf16 v[34:49], v[134:137], v[208:211], v[34:49]
	ds_read_b64_tr_b16 v[196:197], v166 offset:0x4600
	ds_read_b64_tr_b16 v[198:199], v166 offset:0x4e00
	ds_read_b64_tr_b16 v[200:201], v166 offset:0x5600
	ds_read_b64_tr_b16 v[202:203], v166 offset:0x5e00
	ds_read_b64_tr_b16 v[204:205], v166 offset:0x6600
	ds_read_b64_tr_b16 v[206:207], v166 offset:0x6e00
	ds_read_b64_tr_b16 v[208:209], v166 offset:0x7600
	ds_read_b64_tr_b16 v[210:211], v166 offset:0x7e00
	s_waitcnt lgkmcnt(8)
	v_mfma_f32_32x32x16_bf16 v[50:65], v[122:125], v[140:143], v[50:65]
	v_mfma_f32_32x32x16_bf16 v[50:65], v[126:129], v[144:147], v[50:65]
	v_mfma_f32_32x32x16_bf16 v[50:65], v[130:133], v[148:151], v[50:65]
	v_mfma_f32_32x32x16_bf16 v[50:65], v[134:137], v[152:155], v[50:65]
	s_waitcnt lgkmcnt(0)
	v_mfma_f32_32x32x16_bf16 v[2:17], v[122:125], v[196:199], v[2:17]
	s_cmp_le_i32 s95, s77
	v_mfma_f32_32x32x16_bf16 v[2:17], v[126:129], v[200:203], v[2:17]
	v_mfma_f32_32x32x16_bf16 v[2:17], v[130:133], v[204:207], v[2:17]
	v_mfma_f32_32x32x16_bf16 v[2:17], v[134:137], v[208:211], v[2:17]
	s_cbranch_scc1 .LBB0_271
	v_add_u32_e32 v122, 0xffffff40, v183
	v_cmp_gt_i32_e64 s[66:67], 26, v122
	v_cmp_gt_i32_e64 s[68:69], 27, v122
	v_cmp_gt_i32_e64 s[64:65], 25, v122
	s_and_b64 s[66:67], s[68:69], s[66:67]
	v_cmp_gt_i32_e64 s[62:63], 24, v122
	s_and_b64 s[64:65], s[66:67], s[64:65]
	v_cmp_gt_i32_e64 s[60:61], 19, v122
	s_and_b64 s[62:63], s[64:65], s[62:63]
	v_cmp_gt_i32_e64 s[58:59], 18, v122
	s_and_b64 s[60:61], s[62:63], s[60:61]
	v_cmp_gt_i32_e64 s[56:57], 17, v122
	s_and_b64 s[58:59], s[60:61], s[58:59]
	v_cmp_gt_i32_e64 s[54:55], 16, v122
	s_and_b64 s[56:57], s[58:59], s[56:57]
	v_cmp_gt_i32_e64 s[52:53], 11, v122
	s_and_b64 s[54:55], s[56:57], s[54:55]
	v_cmp_gt_i32_e64 s[50:51], 10, v122
	s_and_b64 s[52:53], s[54:55], s[52:53]
	v_cmp_gt_i32_e64 s[48:49], 9, v122
	s_and_b64 s[50:51], s[52:53], s[50:51]
	v_cmp_gt_i32_e64 s[44:45], 8, v122
	s_and_b64 s[48:49], s[50:51], s[48:49]
	v_cmp_gt_i32_e64 s[42:43], 3, v122
	s_and_b64 s[44:45], s[48:49], s[44:45]
	v_cmp_gt_i32_e64 s[40:41], 2, v122
	s_and_b64 s[42:43], s[44:45], s[42:43]
	v_cmp_gt_i32_e64 s[38:39], 1, v122
	s_and_b64 s[40:41], s[42:43], s[40:41]
	v_cmp_gt_i32_e64 s[36:37], 0, v122
	s_and_b64 s[38:39], s[40:41], s[38:39]
	s_and_b64 s[36:37], s[38:39], s[36:37]
	v_cmp_gt_i32_e64 s[34:35], 58, v122
	v_cndmask_b32_e64 v82, v82, v160, s[36:37]
	v_cmp_gt_i32_e64 s[36:37], 59, v122
	v_cmp_gt_i32_e64 s[30:31], 57, v122
	s_and_b64 s[34:35], s[36:37], s[34:35]
	v_cmp_gt_i32_e64 s[28:29], 56, v122
	s_and_b64 s[30:31], s[34:35], s[30:31]
	v_cmp_gt_i32_e64 s[26:27], 51, v122
	s_and_b64 s[28:29], s[30:31], s[28:29]
	v_cmp_gt_i32_e64 s[24:25], 50, v122
	s_and_b64 s[26:27], s[28:29], s[26:27]
	v_cmp_gt_i32_e64 s[22:23], 49, v122
	s_and_b64 s[24:25], s[26:27], s[24:25]
	v_cmp_gt_i32_e64 s[20:21], 48, v122
	s_and_b64 s[22:23], s[24:25], s[22:23]
	v_cmp_gt_i32_e64 s[18:19], 43, v122
	s_and_b64 s[20:21], s[22:23], s[20:21]
	v_cmp_gt_i32_e64 s[16:17], 42, v122
	s_and_b64 s[18:19], s[20:21], s[18:19]
	v_cmp_gt_i32_e64 s[14:15], 41, v122
	s_and_b64 s[16:17], s[18:19], s[16:17]
	v_cmp_gt_i32_e64 s[12:13], 40, v122
	s_and_b64 s[14:15], s[16:17], s[14:15]
	v_cmp_gt_i32_e64 s[10:11], 35, v122
	s_and_b64 s[12:13], s[14:15], s[12:13]
	v_cmp_gt_i32_e64 s[8:9], 34, v122
	s_and_b64 s[10:11], s[12:13], s[10:11]
	v_cmp_gt_i32_e64 s[6:7], 33, v122
	s_and_b64 s[8:9], s[10:11], s[8:9]
	v_cmp_gt_i32_e32 vcc, 32, v122
	s_and_b64 s[6:7], s[8:9], s[6:7]
	s_and_b64 vcc, s[6:7], vcc
	v_cndmask_b32_e64 v97, v97, v160, s[68:69]
	v_cndmask_b32_e64 v96, v96, v160, s[66:67]
	v_cndmask_b32_e64 v95, v95, v160, s[64:65]
	v_cndmask_b32_e64 v94, v94, v160, s[62:63]
	v_cndmask_b32_e64 v93, v93, v160, s[60:61]
	v_cndmask_b32_e64 v92, v92, v160, s[58:59]
	v_cndmask_b32_e64 v91, v91, v160, s[56:57]
	v_cndmask_b32_e64 v90, v90, v160, s[54:55]
	v_cndmask_b32_e64 v89, v89, v160, s[52:53]
	v_cndmask_b32_e64 v88, v88, v160, s[50:51]
	v_cndmask_b32_e64 v87, v87, v160, s[48:49]
	v_cndmask_b32_e64 v86, v86, v160, s[44:45]
	v_cndmask_b32_e64 v85, v85, v160, s[42:43]
	v_cndmask_b32_e64 v84, v84, v160, s[40:41]
	v_cndmask_b32_e64 v83, v83, v160, s[38:39]
	v_cndmask_b32_e64 v81, v81, v160, s[36:37]
	v_cndmask_b32_e64 v80, v80, v160, s[34:35]
	v_cndmask_b32_e64 v79, v79, v160, s[30:31]
	v_cndmask_b32_e64 v78, v78, v160, s[28:29]
	v_cndmask_b32_e64 v77, v77, v160, s[26:27]
	v_cndmask_b32_e64 v76, v76, v160, s[24:25]
	v_cndmask_b32_e64 v75, v75, v160, s[22:23]
	v_cndmask_b32_e64 v74, v74, v160, s[20:21]
	v_cndmask_b32_e64 v73, v73, v160, s[18:19]
	v_cndmask_b32_e64 v72, v72, v160, s[16:17]
	v_cndmask_b32_e64 v71, v71, v160, s[14:15]
	v_cndmask_b32_e64 v70, v70, v160, s[12:13]
	v_cndmask_b32_e64 v69, v69, v160, s[10:11]
	v_cndmask_b32_e64 v68, v68, v160, s[8:9]
	v_cndmask_b32_e64 v67, v67, v160, s[6:7]
	v_cndmask_b32_e32 v66, v66, v160, vcc

.LBB0_275:
	v_mov_b32_e32 v155, v154
	v_mov_b32_e32 v82, v154
	v_mov_b32_e32 v83, v154
	v_pk_fma_f32 v[154:155], v[66:67], s[84:85], v[154:155] op_sel_hi:[1,0,1]
	v_add_f32_e32 v66, v114, v115
	v_fmac_f32_e32 v66, v181, v180
	v_add_f32_e32 v67, v116, v117
	s_addk_i32 s95, 0x100
	v_fmac_f32_e32 v67, v66, v184
	v_add_f32_e32 v66, v120, v186
	s_add_u32 s70, s70, 0x100000
	v_fmac_f32_e32 v66, v67, v185
	v_add_f32_e32 v180, v138, v195
	s_addc_u32 s71, s71, 0
	s_add_i32 s75, s75, 4
	v_pk_fma_f32 v[140:141], v[80:81], s[84:85], v[82:83] op_sel_hi:[1,0,1]
	v_pk_fma_f32 v[142:143], v[78:79], s[84:85], v[82:83] op_sel_hi:[1,0,1]
	v_pk_fma_f32 v[144:145], v[76:77], s[84:85], v[82:83] op_sel_hi:[1,0,1]
	v_pk_fma_f32 v[146:147], v[74:75], s[84:85], v[82:83] op_sel_hi:[1,0,1]
	v_pk_fma_f32 v[148:149], v[72:73], s[84:85], v[82:83] op_sel_hi:[1,0,1]
	v_pk_fma_f32 v[150:151], v[70:71], s[84:85], v[82:83] op_sel_hi:[1,0,1]
	v_pk_fma_f32 v[152:153], v[68:69], s[84:85], v[82:83] op_sel_hi:[1,0,1]
	v_fmac_f32_e32 v180, v66, v187
	s_cmp_ge_u32 s75, s94
	v_add_u32_e32 v183, 0xffffff00, v183
	s_waitcnt vmcnt(0)
	s_barrier
	s_cbranch_scc1 .LBB0_278
	v_mov_b32_e32 v181, v121
	s_branch .LBB0_251
